# cache-policy: out_proj layer-0 f32 residual loads and the final pass's X loads made non-temporal
# baseline (speedup 1.0000x reference)
.LBB0_1396:
	s_add_i32 s19, s27, 0
	s_ashr_i32 s27, s26, 31
	s_add_i32 s19, s19, 0x25000
	s_lshl_b64 s[26:27], s[26:27], 19
	v_lshl_or_b32 v162, s75, 8, v231
	s_add_u32 s26, s66, s26
	v_lshlrev_b32_e32 v130, 2, v231
	s_addc_u32 s27, s67, s27
	s_andn2_b64 vcc, exec, s[16:17]
	v_add_u32_e32 v163, s19, v130
	v_add_u32_e32 v208, v162, v192
	s_cbranch_vccnz .LBB0_1402
	v_ashrrev_i32_e32 v209, 31, v208
	v_lshl_add_u64 v[130:131], v[208:209], 2, s[28:29]
	global_load_dwordx4 v[170:173], v[130:131], off nt
	global_load_dwordx4 v[174:177], v[130:131], off offset:16 nt
	global_load_dwordx4 v[178:181], v[130:131], off offset:512 nt
	global_load_dwordx4 v[182:185], v[130:131], off offset:528 nt
	v_add_u32_e32 v218, 0x4000, v208
	v_ashrrev_i32_e32 v219, 31, v218
	v_lshl_add_u64 v[130:131], v[218:219], 2, s[28:29]
	global_load_dwordx4 v[210:213], v[130:131], off offset:16 nt
	global_load_dwordx4 v[214:217], v[130:131], off nt
	v_add_u32_e32 v168, 0x4080, v208
	v_add_u32_e32 v166, 0x8000, v208
	v_add_u32_e32 v164, 0x8080, v208
	v_add_u32_e32 v160, 0xc000, v208
	v_add_u32_e32 v158, 0xc080, v208
	v_ashrrev_i32_e32 v169, 31, v168
	v_ashrrev_i32_e32 v167, 31, v166
	v_ashrrev_i32_e32 v165, 31, v164
	v_ashrrev_i32_e32 v161, 31, v160
	v_ashrrev_i32_e32 v159, 31, v158
	v_lshl_add_u64 v[130:131], v[168:169], 2, s[28:29]
	v_lshl_add_u64 v[132:133], v[166:167], 2, s[28:29]
	v_lshl_add_u64 v[134:135], v[164:165], 2, s[28:29]
	v_lshl_add_u64 v[136:137], v[160:161], 2, s[28:29]
	v_lshl_add_u64 v[238:239], v[158:159], 2, s[28:29]
	global_load_dwordx4 v[222:225], v[130:131], off offset:16 nt
	global_load_dwordx4 v[226:229], v[130:131], off nt
	global_load_dwordx4 v[154:157], v[132:133], off offset:16 nt
	global_load_dwordx4 v[234:237], v[132:133], off nt
	global_load_dwordx4 v[146:149], v[134:135], off offset:16 nt
	global_load_dwordx4 v[150:153], v[134:135], off nt
	global_load_dwordx4 v[138:141], v[136:137], off offset:16 nt
	global_load_dwordx4 v[142:145], v[136:137], off nt
	s_nop 0
	global_load_dwordx4 v[130:133], v[238:239], off offset:16 nt
	global_load_dwordx4 v[134:137], v[238:239], off nt
	ds_read_b128 v[238:241], v163
	ds_read_b128 v[242:245], v163 offset:1024
	v_lshl_add_u64 v[246:247], v[208:209], 1, s[26:27]
	v_lshl_add_u64 v[168:169], v[168:169], 1, s[26:27]
	v_lshl_add_u64 v[166:167], v[166:167], 1, s[26:27]
	s_waitcnt lgkmcnt(0)
	v_pk_add_f32 v[238:239], v[126:127], v[238:239]
	v_pk_add_f32 v[240:241], v[128:129], v[240:241]
	v_add_u32_e32 v248, 0x24000, v208
	v_ashrrev_i32_e32 v249, 31, v248
	s_waitcnt vmcnt(0)
	v_pk_fma_f32 v[170:171], v[242:243], v[238:239], v[170:171]
	v_pk_fma_f32 v[172:173], v[244:245], v[240:241], v[172:173]
	v_cvt_pk_bf16_f32 v170, v170, v171
	s_nop 0
	v_cvt_pk_bf16_f32 v171, v172, v173
	ds_read_b128 v[238:241], v163 offset:16
	ds_read_b128 v[242:245], v163 offset:1040
	s_waitcnt lgkmcnt(1)
	v_pk_add_f32 v[172:173], v[124:125], v[240:241]
	v_pk_add_f32 v[238:239], v[122:123], v[238:239]
	s_waitcnt lgkmcnt(0)
	v_pk_fma_f32 v[176:177], v[244:245], v[172:173], v[176:177]
	v_pk_fma_f32 v[172:173], v[242:243], v[238:239], v[174:175]
	s_nop 0
	v_cvt_pk_bf16_f32 v172, v172, v173
	v_cvt_pk_bf16_f32 v173, v176, v177
	global_store_dwordx4 v[246:247], v[170:173], off
	ds_read_b128 v[170:173], v163 offset:512
	ds_read_b128 v[174:177], v163 offset:1536
	s_waitcnt lgkmcnt(1)
	v_pk_add_f32 v[172:173], v[120:121], v[172:173]
	v_pk_add_f32 v[170:171], v[118:119], v[170:171]
	s_waitcnt lgkmcnt(0)
	v_pk_fma_f32 v[172:173], v[176:177], v[172:173], v[180:181]
	v_pk_fma_f32 v[170:171], v[174:175], v[170:171], v[178:179]
	v_lshl_add_u64 v[180:181], v[218:219], 1, s[26:27]
	v_cvt_pk_bf16_f32 v170, v170, v171
	v_cvt_pk_bf16_f32 v171, v172, v173
	ds_read_b128 v[172:175], v163 offset:528
	ds_read_b128 v[176:179], v163 offset:1552
	v_add_u32_e32 v218, 0x20000, v208
	v_ashrrev_i32_e32 v219, 31, v218
	s_waitcnt lgkmcnt(1)
	v_pk_add_f32 v[172:173], v[114:115], v[172:173]
	v_pk_add_f32 v[174:175], v[116:117], v[174:175]
	s_waitcnt lgkmcnt(0)
	v_pk_fma_f32 v[172:173], v[176:177], v[172:173], v[182:183]
	v_pk_fma_f32 v[174:175], v[178:179], v[174:175], v[184:185]
	v_cvt_pk_bf16_f32 v172, v172, v173
	s_nop 0
	v_cvt_pk_bf16_f32 v173, v174, v175
	global_store_dwordx4 v[246:247], v[170:173], off offset:256
	ds_read_b128 v[170:173], v163
	ds_read_b128 v[174:177], v163 offset:1024
	v_add_u32_e32 v246, 0x20080, v208
	v_ashrrev_i32_e32 v247, 31, v246
	s_waitcnt lgkmcnt(1)
	v_pk_add_f32 v[172:173], v[112:113], v[172:173]
	v_pk_add_f32 v[170:171], v[110:111], v[170:171]
	s_waitcnt lgkmcnt(0)
	v_pk_fma_f32 v[172:173], v[176:177], v[172:173], v[216:217]
	v_pk_fma_f32 v[170:171], v[174:175], v[170:171], v[214:215]
	s_nop 0
	v_cvt_pk_bf16_f32 v170, v170, v171
	v_cvt_pk_bf16_f32 v171, v172, v173
	ds_read_b128 v[172:175], v163 offset:16
	ds_read_b128 v[176:179], v163 offset:1040
	s_waitcnt lgkmcnt(1)
	v_pk_add_f32 v[172:173], v[106:107], v[172:173]
	v_pk_add_f32 v[174:175], v[108:109], v[174:175]
	s_waitcnt lgkmcnt(0)
	v_pk_fma_f32 v[172:173], v[176:177], v[172:173], v[210:211]
	v_pk_fma_f32 v[174:175], v[178:179], v[174:175], v[212:213]
	v_cvt_pk_bf16_f32 v172, v172, v173
	s_nop 0
	v_cvt_pk_bf16_f32 v173, v174, v175
	global_store_dwordx4 v[180:181], v[170:173], off
	ds_read_b128 v[170:173], v163 offset:512
	ds_read_b128 v[174:177], v163 offset:1536
	s_waitcnt lgkmcnt(1)
	v_pk_add_f32 v[172:173], v[104:105], v[172:173]
	v_pk_add_f32 v[170:171], v[102:103], v[170:171]
	s_waitcnt lgkmcnt(0)
	v_pk_fma_f32 v[172:173], v[176:177], v[172:173], v[228:229]
	v_pk_fma_f32 v[170:171], v[174:175], v[170:171], v[226:227]
	s_nop 0
	v_cvt_pk_bf16_f32 v170, v170, v171
	v_cvt_pk_bf16_f32 v171, v172, v173
	ds_read_b128 v[172:175], v163 offset:528
	ds_read_b128 v[176:179], v163 offset:1552
	s_waitcnt lgkmcnt(1)
	v_pk_add_f32 v[172:173], v[98:99], v[172:173]
	v_pk_add_f32 v[174:175], v[100:101], v[174:175]
	s_waitcnt lgkmcnt(0)
	v_pk_fma_f32 v[172:173], v[176:177], v[172:173], v[222:223]
	v_pk_fma_f32 v[174:175], v[178:179], v[174:175], v[224:225]
	v_cvt_pk_bf16_f32 v172, v172, v173
	s_nop 0
	v_cvt_pk_bf16_f32 v173, v174, v175
	global_store_dwordx4 v[168:169], v[170:173], off
	ds_read_b128 v[168:171], v163
	ds_read_b128 v[172:175], v163 offset:1024
	s_waitcnt lgkmcnt(1)
	v_pk_add_f32 v[170:171], v[96:97], v[170:171]
	v_pk_add_f32 v[168:169], v[94:95], v[168:169]
	s_waitcnt lgkmcnt(0)
	v_pk_fma_f32 v[170:171], v[174:175], v[170:171], v[236:237]
	v_pk_fma_f32 v[168:169], v[172:173], v[168:169], v[234:235]
	s_nop 0
	v_cvt_pk_bf16_f32 v168, v168, v169
	v_cvt_pk_bf16_f32 v169, v170, v171
	ds_read_b128 v[170:173], v163 offset:16
	ds_read_b128 v[174:177], v163 offset:1040
	s_waitcnt lgkmcnt(1)
	v_pk_add_f32 v[172:173], v[92:93], v[172:173]
	v_pk_add_f32 v[170:171], v[90:91], v[170:171]
	s_waitcnt lgkmcnt(0)
	v_pk_fma_f32 v[156:157], v[176:177], v[172:173], v[156:157]
	v_pk_fma_f32 v[154:155], v[174:175], v[170:171], v[154:155]
	s_nop 0
	v_cvt_pk_bf16_f32 v170, v154, v155
	v_cvt_pk_bf16_f32 v171, v156, v157
	global_store_dwordx4 v[166:167], v[168:171], off
	ds_read_b128 v[154:157], v163 offset:512
	ds_read_b128 v[166:169], v163 offset:1536
	s_waitcnt lgkmcnt(1)
	v_pk_add_f32 v[156:157], v[88:89], v[156:157]
	v_pk_add_f32 v[154:155], v[86:87], v[154:155]
	s_waitcnt lgkmcnt(0)
	v_pk_fma_f32 v[152:153], v[168:169], v[156:157], v[152:153]
	v_pk_fma_f32 v[150:151], v[166:167], v[154:155], v[150:151]
	v_lshl_add_u64 v[156:157], v[164:165], 1, s[26:27]
	v_cvt_pk_bf16_f32 v150, v150, v151
	v_cvt_pk_bf16_f32 v151, v152, v153
	ds_read_b128 v[152:155], v163 offset:528
	ds_read_b128 v[166:169], v163 offset:1552
	v_add_u32_e32 v164, 0x28080, v208
	v_ashrrev_i32_e32 v165, 31, v164
	s_waitcnt lgkmcnt(1)
	v_pk_add_f32 v[154:155], v[84:85], v[154:155]
	v_pk_add_f32 v[152:153], v[82:83], v[152:153]
	s_waitcnt lgkmcnt(0)
	v_pk_fma_f32 v[148:149], v[168:169], v[154:155], v[148:149]
	v_pk_fma_f32 v[146:147], v[166:167], v[152:153], v[146:147]
	v_add_u32_e32 v168, 0x24080, v208
	v_cvt_pk_bf16_f32 v152, v146, v147
	v_cvt_pk_bf16_f32 v153, v148, v149
	global_store_dwordx4 v[156:157], v[150:153], off
	ds_read_b128 v[146:149], v163
	ds_read_b128 v[150:153], v163 offset:1024
	v_add_u32_e32 v166, 0x28000, v208
	v_ashrrev_i32_e32 v169, 31, v168
	v_ashrrev_i32_e32 v167, 31, v166
	s_waitcnt lgkmcnt(1)
	v_pk_add_f32 v[148:149], v[80:81], v[148:149]
	v_pk_add_f32 v[146:147], v[78:79], v[146:147]
	s_waitcnt lgkmcnt(0)
	v_pk_fma_f32 v[144:145], v[152:153], v[148:149], v[144:145]
	v_pk_fma_f32 v[142:143], v[150:151], v[146:147], v[142:143]
	v_lshl_add_u64 v[152:153], v[160:161], 1, s[26:27]
	v_cvt_pk_bf16_f32 v142, v142, v143
	v_cvt_pk_bf16_f32 v143, v144, v145
	ds_read_b128 v[144:147], v163 offset:16
	ds_read_b128 v[148:151], v163 offset:1040
	v_add_u32_e32 v160, 0x2c000, v208
	v_ashrrev_i32_e32 v161, 31, v160
	s_waitcnt lgkmcnt(1)
	v_pk_add_f32 v[146:147], v[76:77], v[146:147]
	v_pk_add_f32 v[144:145], v[74:75], v[144:145]
	s_waitcnt lgkmcnt(0)
	v_pk_fma_f32 v[140:141], v[150:151], v[146:147], v[140:141]
	v_pk_fma_f32 v[138:139], v[148:149], v[144:145], v[138:139]
	v_lshl_add_u64 v[146:147], v[218:219], 2, s[28:29]
	v_cvt_pk_bf16_f32 v144, v138, v139
	v_cvt_pk_bf16_f32 v145, v140, v141
	global_store_dwordx4 v[152:153], v[142:145], off
	ds_read_b128 v[138:141], v163 offset:512
	ds_read_b128 v[142:145], v163 offset:1536
	v_lshl_add_u64 v[218:219], v[218:219], 1, s[26:27]
	s_waitcnt lgkmcnt(1)
	v_pk_add_f32 v[140:141], v[72:73], v[140:141]
	v_pk_add_f32 v[138:139], v[70:71], v[138:139]
	s_waitcnt lgkmcnt(0)
	v_pk_fma_f32 v[136:137], v[144:145], v[140:141], v[136:137]
	v_pk_fma_f32 v[134:135], v[142:143], v[138:139], v[134:135]
	v_lshl_add_u64 v[144:145], v[158:159], 1, s[26:27]
	v_cvt_pk_bf16_f32 v134, v134, v135
	v_cvt_pk_bf16_f32 v135, v136, v137
	ds_read_b128 v[136:139], v163 offset:528
	ds_read_b128 v[140:143], v163 offset:1552
	v_add_u32_e32 v158, 0x2c080, v208
	v_ashrrev_i32_e32 v159, 31, v158
	v_lshl_add_u64 v[238:239], v[158:159], 2, s[28:29]
	s_waitcnt lgkmcnt(1)
	v_pk_add_f32 v[138:139], v[68:69], v[138:139]
	v_pk_add_f32 v[136:137], v[66:67], v[136:137]
	s_waitcnt lgkmcnt(0)
	v_pk_fma_f32 v[132:133], v[142:143], v[138:139], v[132:133]
	v_pk_fma_f32 v[130:131], v[140:141], v[136:137], v[130:131]
	s_nop 0
	v_cvt_pk_bf16_f32 v136, v130, v131
	v_cvt_pk_bf16_f32 v137, v132, v133
	global_store_dwordx4 v[144:145], v[134:137], off
	global_load_dwordx4 v[170:173], v[146:147], off nt
	global_load_dwordx4 v[174:177], v[146:147], off offset:16 nt
	v_lshl_add_u64 v[130:131], v[246:247], 2, s[28:29]
	global_load_dwordx4 v[178:181], v[130:131], off nt
	global_load_dwordx4 v[182:185], v[130:131], off offset:16 nt
	v_lshl_add_u64 v[130:131], v[248:249], 2, s[28:29]
	global_load_dwordx4 v[210:213], v[130:131], off offset:16 nt
	global_load_dwordx4 v[214:217], v[130:131], off nt
	v_lshl_add_u64 v[130:131], v[168:169], 2, s[28:29]
	v_lshl_add_u64 v[132:133], v[166:167], 2, s[28:29]
	v_lshl_add_u64 v[134:135], v[164:165], 2, s[28:29]
	v_lshl_add_u64 v[136:137], v[160:161], 2, s[28:29]
	global_load_dwordx4 v[222:225], v[130:131], off offset:16 nt
	global_load_dwordx4 v[226:229], v[130:131], off nt
	global_load_dwordx4 v[154:157], v[132:133], off offset:16 nt
	global_load_dwordx4 v[234:237], v[132:133], off nt
	global_load_dwordx4 v[146:149], v[134:135], off offset:16 nt
	global_load_dwordx4 v[150:153], v[134:135], off nt
	global_load_dwordx4 v[138:141], v[136:137], off offset:16 nt
	global_load_dwordx4 v[142:145], v[136:137], off nt
	s_nop 0
	global_load_dwordx4 v[130:133], v[238:239], off offset:16 nt
	global_load_dwordx4 v[134:137], v[238:239], off nt
	ds_read_b128 v[238:241], v163
	ds_read_b128 v[242:245], v163 offset:1024
	v_lshl_add_u64 v[168:169], v[168:169], 1, s[26:27]
	v_lshl_add_u64 v[166:167], v[166:167], 1, s[26:27]
	s_waitcnt lgkmcnt(1)
	v_pk_add_f32 v[238:239], v[62:63], v[238:239]
	v_pk_add_f32 v[240:241], v[64:65], v[240:241]
	s_waitcnt vmcnt(15) lgkmcnt(0)
	v_pk_fma_f32 v[170:171], v[242:243], v[238:239], v[170:171]
	v_pk_fma_f32 v[172:173], v[244:245], v[240:241], v[172:173]
	v_cvt_pk_bf16_f32 v170, v170, v171
	s_nop 0
	v_cvt_pk_bf16_f32 v171, v172, v173
	ds_read_b128 v[238:241], v163 offset:16
	ds_read_b128 v[242:245], v163 offset:1040
	s_waitcnt lgkmcnt(1)
	v_pk_add_f32 v[172:173], v[60:61], v[240:241]
	v_pk_add_f32 v[238:239], v[58:59], v[238:239]
	s_waitcnt vmcnt(14) lgkmcnt(0)
	v_pk_fma_f32 v[176:177], v[244:245], v[172:173], v[176:177]
	v_pk_fma_f32 v[172:173], v[242:243], v[238:239], v[174:175]
	s_nop 0
	v_cvt_pk_bf16_f32 v172, v172, v173
	v_cvt_pk_bf16_f32 v173, v176, v177
	global_store_dwordx4 v[218:219], v[170:173], off
	ds_read_b128 v[170:173], v163 offset:512
	ds_read_b128 v[174:177], v163 offset:1536
	s_waitcnt lgkmcnt(1)
	v_pk_add_f32 v[172:173], v[56:57], v[172:173]
	v_pk_add_f32 v[170:171], v[54:55], v[170:171]
	s_waitcnt vmcnt(14) lgkmcnt(0)
	v_pk_fma_f32 v[172:173], v[176:177], v[172:173], v[180:181]
	v_pk_fma_f32 v[170:171], v[174:175], v[170:171], v[178:179]
	v_lshl_add_u64 v[180:181], v[246:247], 1, s[26:27]
	v_cvt_pk_bf16_f32 v170, v170, v171
	v_cvt_pk_bf16_f32 v171, v172, v173
	ds_read_b128 v[172:175], v163 offset:528
	ds_read_b128 v[176:179], v163 offset:1552
	s_waitcnt lgkmcnt(1)
	v_pk_add_f32 v[172:173], v[50:51], v[172:173]
	v_pk_add_f32 v[174:175], v[52:53], v[174:175]
	s_waitcnt vmcnt(13) lgkmcnt(0)
	v_pk_fma_f32 v[172:173], v[176:177], v[172:173], v[182:183]
	v_pk_fma_f32 v[174:175], v[178:179], v[174:175], v[184:185]
	v_cvt_pk_bf16_f32 v172, v172, v173
	s_nop 0
	v_cvt_pk_bf16_f32 v173, v174, v175
	global_store_dwordx4 v[180:181], v[170:173], off
	ds_read_b128 v[170:173], v163
	ds_read_b128 v[174:177], v163 offset:1024
	v_lshl_add_u64 v[180:181], v[248:249], 1, s[26:27]
	s_waitcnt lgkmcnt(1)
	v_pk_add_f32 v[172:173], v[48:49], v[172:173]
	v_pk_add_f32 v[170:171], v[46:47], v[170:171]
	s_waitcnt vmcnt(12) lgkmcnt(0)
	v_pk_fma_f32 v[172:173], v[176:177], v[172:173], v[216:217]
	v_pk_fma_f32 v[170:171], v[174:175], v[170:171], v[214:215]
	s_nop 0
	v_cvt_pk_bf16_f32 v170, v170, v171
	v_cvt_pk_bf16_f32 v171, v172, v173
	ds_read_b128 v[172:175], v163 offset:16
	ds_read_b128 v[176:179], v163 offset:1040
	s_waitcnt lgkmcnt(1)
	v_pk_add_f32 v[172:173], v[42:43], v[172:173]
	v_pk_add_f32 v[174:175], v[44:45], v[174:175]
	s_waitcnt lgkmcnt(0)
	v_pk_fma_f32 v[172:173], v[176:177], v[172:173], v[210:211]
	v_pk_fma_f32 v[174:175], v[178:179], v[174:175], v[212:213]
	v_cvt_pk_bf16_f32 v172, v172, v173
	s_nop 0
	v_cvt_pk_bf16_f32 v173, v174, v175
	global_store_dwordx4 v[180:181], v[170:173], off
	ds_read_b128 v[170:173], v163 offset:512
	ds_read_b128 v[174:177], v163 offset:1536
	s_waitcnt lgkmcnt(1)
	v_pk_add_f32 v[172:173], v[40:41], v[172:173]
	v_pk_add_f32 v[170:171], v[38:39], v[170:171]
	s_waitcnt vmcnt(11) lgkmcnt(0)
	v_pk_fma_f32 v[172:173], v[176:177], v[172:173], v[228:229]
	v_pk_fma_f32 v[170:171], v[174:175], v[170:171], v[226:227]
	s_nop 0
	v_cvt_pk_bf16_f32 v170, v170, v171
	v_cvt_pk_bf16_f32 v171, v172, v173
	ds_read_b128 v[172:175], v163 offset:528
	ds_read_b128 v[176:179], v163 offset:1552
	s_waitcnt lgkmcnt(1)
	v_pk_add_f32 v[172:173], v[34:35], v[172:173]
	v_pk_add_f32 v[174:175], v[36:37], v[174:175]
	s_waitcnt lgkmcnt(0)
	v_pk_fma_f32 v[172:173], v[176:177], v[172:173], v[222:223]
	v_pk_fma_f32 v[174:175], v[178:179], v[174:175], v[224:225]
	v_cvt_pk_bf16_f32 v172, v172, v173
	s_nop 0
	v_cvt_pk_bf16_f32 v173, v174, v175
	global_store_dwordx4 v[168:169], v[170:173], off
	ds_read_b128 v[168:171], v163
	ds_read_b128 v[172:175], v163 offset:1024
	s_waitcnt lgkmcnt(1)
	v_pk_add_f32 v[170:171], v[32:33], v[170:171]
	v_pk_add_f32 v[168:169], v[30:31], v[168:169]
	s_waitcnt vmcnt(10) lgkmcnt(0)
	v_pk_fma_f32 v[170:171], v[174:175], v[170:171], v[236:237]
	v_pk_fma_f32 v[168:169], v[172:173], v[168:169], v[234:235]
	s_nop 0
	v_cvt_pk_bf16_f32 v168, v168, v169
	v_cvt_pk_bf16_f32 v169, v170, v171
	ds_read_b128 v[170:173], v163 offset:16
	ds_read_b128 v[174:177], v163 offset:1040
	s_waitcnt lgkmcnt(1)
	v_pk_add_f32 v[172:173], v[28:29], v[172:173]
	v_pk_add_f32 v[170:171], v[26:27], v[170:171]
	s_waitcnt lgkmcnt(0)
	v_pk_fma_f32 v[156:157], v[176:177], v[172:173], v[156:157]
	v_pk_fma_f32 v[154:155], v[174:175], v[170:171], v[154:155]
	s_nop 0
	v_cvt_pk_bf16_f32 v170, v154, v155
	v_cvt_pk_bf16_f32 v171, v156, v157
	global_store_dwordx4 v[166:167], v[168:171], off
	ds_read_b128 v[154:157], v163 offset:512
	ds_read_b128 v[166:169], v163 offset:1536
	s_waitcnt lgkmcnt(1)
	v_pk_add_f32 v[156:157], v[24:25], v[156:157]
	v_pk_add_f32 v[154:155], v[22:23], v[154:155]
	s_waitcnt vmcnt(9) lgkmcnt(0)
	v_pk_fma_f32 v[152:153], v[168:169], v[156:157], v[152:153]
	v_pk_fma_f32 v[150:151], v[166:167], v[154:155], v[150:151]
	v_lshl_add_u64 v[156:157], v[164:165], 1, s[26:27]
	v_cvt_pk_bf16_f32 v150, v150, v151
	v_cvt_pk_bf16_f32 v151, v152, v153
	ds_read_b128 v[152:155], v163 offset:528
	ds_read_b128 v[166:169], v163 offset:1552
	s_waitcnt lgkmcnt(1)
	v_pk_add_f32 v[154:155], v[20:21], v[154:155]
	v_pk_add_f32 v[152:153], v[18:19], v[152:153]
	s_waitcnt lgkmcnt(0)
	v_pk_fma_f32 v[148:149], v[168:169], v[154:155], v[148:149]
	v_pk_fma_f32 v[146:147], v[166:167], v[152:153], v[146:147]
	s_nop 0
	v_cvt_pk_bf16_f32 v152, v146, v147
	v_cvt_pk_bf16_f32 v153, v148, v149
	global_store_dwordx4 v[156:157], v[150:153], off
	ds_read_b128 v[146:149], v163
	ds_read_b128 v[150:153], v163 offset:1024
	s_waitcnt lgkmcnt(1)
	v_pk_add_f32 v[148:149], v[16:17], v[148:149]
	v_pk_add_f32 v[146:147], v[14:15], v[146:147]
	s_waitcnt vmcnt(8) lgkmcnt(0)
	v_pk_fma_f32 v[144:145], v[152:153], v[148:149], v[144:145]
	v_pk_fma_f32 v[142:143], v[150:151], v[146:147], v[142:143]
	v_lshl_add_u64 v[152:153], v[160:161], 1, s[26:27]
	v_cvt_pk_bf16_f32 v142, v142, v143
	v_cvt_pk_bf16_f32 v143, v144, v145
	ds_read_b128 v[144:147], v163 offset:16
	ds_read_b128 v[148:151], v163 offset:1040
	s_waitcnt lgkmcnt(1)
	v_pk_add_f32 v[146:147], v[12:13], v[146:147]
	v_pk_add_f32 v[144:145], v[10:11], v[144:145]
	s_waitcnt lgkmcnt(0)
	v_pk_fma_f32 v[140:141], v[150:151], v[146:147], v[140:141]
	v_pk_fma_f32 v[138:139], v[148:149], v[144:145], v[138:139]
	s_nop 0
	v_cvt_pk_bf16_f32 v144, v138, v139
	v_cvt_pk_bf16_f32 v145, v140, v141
	global_store_dwordx4 v[152:153], v[142:145], off
	ds_read_b128 v[138:141], v163 offset:512
	ds_read_b128 v[142:145], v163 offset:1536
	s_waitcnt lgkmcnt(1)
	v_pk_add_f32 v[140:141], v[8:9], v[140:141]
	v_pk_add_f32 v[138:139], v[6:7], v[138:139]
	s_waitcnt vmcnt(7) lgkmcnt(0)
	v_pk_fma_f32 v[136:137], v[144:145], v[140:141], v[136:137]
	v_pk_fma_f32 v[134:135], v[142:143], v[138:139], v[134:135]
	s_nop 0
	v_cvt_pk_bf16_f32 v134, v134, v135
	v_cvt_pk_bf16_f32 v135, v136, v137
	ds_read_b128 v[136:139], v163 offset:528
	ds_read_b128 v[140:143], v163 offset:1552
	s_waitcnt lgkmcnt(1)
	v_pk_add_f32 v[138:139], v[4:5], v[138:139]
	v_pk_add_f32 v[136:137], v[2:3], v[136:137]
	s_waitcnt lgkmcnt(0)
	v_pk_fma_f32 v[132:133], v[142:143], v[138:139], v[132:133]
	v_pk_fma_f32 v[130:131], v[140:141], v[136:137], v[130:131]
	s_nop 0
	v_cvt_pk_bf16_f32 v136, v130, v131
	v_cvt_pk_bf16_f32 v137, v132, v133
	s_cbranch_execnz .LBB0_1399

.LBB0_1977:
	v_ashrrev_i32_e32 v66, 12, v72
	v_and_b32_e32 v67, 0xffc, v72
	s_waitcnt vmcnt(7)
	v_ashrrev_i32_e32 v49, 31, v44
	v_mov_b32_e32 v48, v44
	v_ashrrev_i32_e32 v51, 31, v45
	v_mov_b32_e32 v50, v45
	v_ashrrev_i32_e32 v45, 31, v46
	v_mov_b32_e32 v44, v46
	v_ashrrev_i32_e32 v53, 31, v47
	v_mov_b32_e32 v52, v47
	s_waitcnt vmcnt(5)
	v_ashrrev_i32_e32 v47, 31, v40
	v_mov_b32_e32 v46, v40
	v_ashrrev_i32_e32 v55, 31, v41
	v_mov_b32_e32 v54, v41
	v_ashrrev_i32_e32 v41, 31, v42
	v_mov_b32_e32 v40, v42
	v_ashrrev_i32_e32 v57, 31, v43
	v_mov_b32_e32 v56, v43
	s_waitcnt vmcnt(3)
	v_ashrrev_i32_e32 v43, 31, v32
	v_mov_b32_e32 v42, v32
	v_ashrrev_i32_e32 v59, 31, v33
	v_mov_b32_e32 v58, v33
	v_ashrrev_i32_e32 v33, 31, v34
	v_mov_b32_e32 v32, v34
	v_mad_i32_i24 v82, v66, s47, v67
	v_add_u32_e32 v80, s78, v72
	v_ashrrev_i32_e32 v61, 31, v35
	v_mov_b32_e32 v60, v35
	s_waitcnt vmcnt(0)
	v_ashrrev_i32_e32 v35, 31, v36
	v_mov_b32_e32 v34, v36
	v_ashrrev_i32_e32 v63, 31, v37
	v_mov_b32_e32 v62, v37
	v_ashrrev_i32_e32 v37, 31, v38
	v_mov_b32_e32 v36, v38
	v_lshlrev_b64 v[116:117], 10, v[32:33]
	v_ashrrev_i32_e32 v83, 31, v82
	v_or_b32_e32 v32, 1, v82
	v_cmp_gt_i32_e64 s[2:3], s71, v80
	v_lshlrev_b64 v[156:157], 10, v[40:41]
	v_lshlrev_b64 v[70:71], 10, v[34:35]
	v_lshlrev_b64 v[66:67], 10, v[36:37]
	v_or_b32_e32 v34, 2, v82
	v_or_b32_e32 v36, 3, v82
	v_lshlrev_b64 v[40:41], 11, v[82:83]
	v_ashrrev_i32_e32 v33, 31, v32
	v_ashrrev_i32_e32 v65, 31, v39
	v_mov_b32_e32 v64, v39
	v_and_b32_e32 v81, 0xfffff000, v72
	v_cndmask_b32_e64 v86, v72, v80, s[2:3]
	v_ashrrev_i32_e32 v35, 31, v34
	v_ashrrev_i32_e32 v37, 31, v36
	v_lshl_add_u64 v[40:41], v[76:77], 0, v[40:41]
	v_lshlrev_b64 v[32:33], 11, v[32:33]
	v_cmp_lt_i32_e32 vcc, s70, v80
	v_lshlrev_b64 v[152:153], 10, v[42:43]
	v_lshlrev_b64 v[96:97], 10, v[64:65]
	v_add_u32_e32 v168, v167, v81
	v_mov_b32_e32 v72, v80
	v_ashrrev_i32_e32 v42, 12, v86
	v_and_b32_e32 v43, 0xffc, v86
	v_lshlrev_b64 v[34:35], 11, v[34:35]
	v_lshlrev_b64 v[36:37], 11, v[36:37]
	global_load_dwordx2 v[64:65], v[40:41], off nt
	global_load_dwordx2 v[80:81], v[40:41], off offset:512 nt
	global_load_dwordx2 v[82:83], v[40:41], off offset:1024 nt
	global_load_dwordx2 v[86:87], v[40:41], off offset:1536 nt
	v_lshl_add_u64 v[32:33], v[76:77], 0, v[32:33]
	s_mov_b32 s10, 35
	v_lshl_add_u64 v[34:35], v[76:77], 0, v[34:35]
	v_lshl_add_u64 v[36:37], v[76:77], 0, v[36:37]
	global_load_dwordx2 v[88:89], v[32:33], off nt
	global_load_dwordx2 v[90:91], v[32:33], off offset:512 nt
	global_load_dwordx2 v[92:93], v[32:33], off offset:1024 nt
	global_load_dwordx2 v[94:95], v[32:33], off offset:1536 nt
	global_load_dwordx2 v[100:101], v[34:35], off nt
	global_load_dwordx2 v[104:105], v[34:35], off offset:512 nt
	global_load_dwordx2 v[108:109], v[34:35], off offset:1024 nt
	global_load_dwordx2 v[112:113], v[34:35], off offset:1536 nt
	global_load_dwordx2 v[174:175], v[36:37], off nt
	global_load_dwordx2 v[176:177], v[36:37], off offset:512 nt
	global_load_dwordx2 v[178:179], v[36:37], off offset:1024 nt
	global_load_dwordx2 v[180:181], v[36:37], off offset:1536 nt
	s_ashr_i32 s11, s10, 31
	s_lshl_b64 s[2:3], s[10:11], 3
	s_add_u32 s2, s0, s2
	s_mov_b32 s14, 35
	s_addc_u32 s3, s1, s3
	s_load_dwordx2 s[2:3], s[2:3], 0x0
	s_ashr_i32 s15, s14, 31
	s_lshl_b64 s[10:11], s[14:15], 3
	s_add_u32 s10, s0, s10
	v_mul_i32_i24_e32 v42, 0x1100, v42
	s_addc_u32 s11, s1, s11
	v_add_lshl_u32 v42, v42, v43, 2
	s_load_dwordx2 s[10:11], s[10:11], 0x0
	v_ashrrev_i32_e32 v43, 31, v42
	v_or_b32_e32 v40, 4, v42
	v_lshlrev_b64 v[32:33], 2, v[42:43]
	v_ashrrev_i32_e32 v41, 31, v40
	v_lshlrev_b64 v[34:35], 2, v[40:41]
	s_waitcnt lgkmcnt(0)
	v_lshl_add_u64 v[40:41], s[2:3], 0, v[32:33]
	v_add_co_u32_e64 v40, s[2:3], s33, v40
	v_lshl_add_u64 v[32:33], s[10:11], 0, v[32:33]
	s_nop 0
	v_addc_co_u32_e64 v41, s[2:3], 0, v41, s[2:3]
	v_lshlrev_b64 v[162:163], 10, v[44:45]
	v_lshlrev_b64 v[158:159], 10, v[46:47]
	v_or_b32_e32 v44, 8, v42
	v_or_b32_e32 v46, 12, v42
	v_add_co_u32_e64 v32, s[2:3], s46, v32
	s_mov_b32 s18, 35
	v_ashrrev_i32_e32 v45, 31, v44
	v_ashrrev_i32_e32 v47, 31, v46
	v_addc_co_u32_e64 v33, s[2:3], 0, v33, s[2:3]
	v_lshlrev_b64 v[84:85], 10, v[48:49]
	v_lshlrev_b64 v[114:115], 10, v[60:61]
	v_lshlrev_b64 v[68:69], 10, v[62:63]
	v_lshlrev_b64 v[36:37], 2, v[44:45]
	v_lshlrev_b64 v[48:49], 2, v[46:47]
	global_load_dwordx4 v[44:47], v[40:41], off
	global_load_dwordx4 v[60:63], v[32:33], off
	s_ashr_i32 s19, s18, 31
	s_lshl_b64 s[2:3], s[18:19], 3
	s_add_u32 s2, s0, s2
	s_mov_b32 s22, 35
	s_addc_u32 s3, s1, s3
	s_load_dwordx2 s[2:3], s[2:3], 0x0
	s_ashr_i32 s23, s22, 31
	s_lshl_b64 s[10:11], s[22:23], 3
	s_add_u32 s10, s0, s10
	s_addc_u32 s11, s1, s11
	s_load_dwordx2 s[10:11], s[10:11], 0x0
	s_waitcnt lgkmcnt(0)
	v_lshl_add_u64 v[32:33], s[2:3], 0, v[34:35]
	v_add_co_u32_e64 v32, s[2:3], s33, v32
	s_mov_b32 s26, 35
	s_nop 0
	v_addc_co_u32_e64 v33, s[2:3], 0, v33, s[2:3]
	global_load_dwordx4 v[40:43], v[32:33], off
	v_lshl_add_u64 v[32:33], s[10:11], 0, v[34:35]
	v_add_co_u32_e64 v32, s[2:3], s46, v32
	v_lshlrev_b64 v[154:155], 10, v[56:57]
	s_nop 0
	v_addc_co_u32_e64 v33, s[2:3], 0, v33, s[2:3]
	v_lshlrev_b64 v[150:151], 10, v[58:59]
	global_load_dwordx4 v[56:59], v[32:33], off
	s_ashr_i32 s27, s26, 31
	s_lshl_b64 s[2:3], s[26:27], 3
	s_add_u32 s2, s0, s2
	s_mov_b32 s36, 35
	s_addc_u32 s3, s1, s3
	s_load_dwordx2 s[2:3], s[2:3], 0x0
	s_ashr_i32 s37, s36, 31
	s_lshl_b64 s[10:11], s[36:37], 3
	s_add_u32 s10, s0, s10
	s_addc_u32 s11, s1, s11
	s_load_dwordx2 s[10:11], s[10:11], 0x0
	s_waitcnt lgkmcnt(0)
	v_lshl_add_u64 v[32:33], s[2:3], 0, v[36:37]
	v_add_co_u32_e64 v32, s[2:3], s33, v32
	s_mov_b32 s42, 35
	s_nop 0
	v_addc_co_u32_e64 v33, s[2:3], 0, v33, s[2:3]
	v_lshl_add_u64 v[36:37], s[10:11], 0, v[36:37]
	v_add_co_u32_e64 v36, s[2:3], s46, v36
	v_lshlrev_b64 v[160:161], 10, v[52:53]
	s_nop 0
	v_addc_co_u32_e64 v37, s[2:3], 0, v37, s[2:3]
	v_lshlrev_b64 v[38:39], 10, v[54:55]
	global_load_dwordx4 v[32:35], v[32:33], off
	s_mov_b32 s52, 35
	global_load_dwordx4 v[52:55], v[36:37], off
	s_ashr_i32 s43, s42, 31
	s_lshl_b64 s[2:3], s[42:43], 3
	s_add_u32 s2, s0, s2
	s_addc_u32 s3, s1, s3
	s_load_dwordx2 s[2:3], s[2:3], 0x0
	s_ashr_i32 s53, s52, 31
	s_lshl_b64 s[10:11], s[52:53], 3
	s_add_u32 s10, s0, s10
	s_addc_u32 s11, s1, s11
	s_load_dwordx2 s[10:11], s[10:11], 0x0
	s_waitcnt lgkmcnt(0)
	v_lshl_add_u64 v[36:37], s[2:3], 0, v[48:49]
	v_add_co_u32_e64 v36, s[2:3], s33, v36
	s_mov_b32 s58, 35
	s_nop 0
	v_addc_co_u32_e64 v37, s[2:3], 0, v37, s[2:3]
	global_load_dwordx4 v[170:173], v[36:37], off
	v_lshl_add_u64 v[36:37], s[10:11], 0, v[48:49]
	v_add_co_u32_e64 v36, s[2:3], s46, v36
	v_lshlrev_b64 v[164:165], 10, v[50:51]
	s_nop 0
	v_addc_co_u32_e64 v37, s[2:3], 0, v37, s[2:3]
	global_load_dwordx4 v[48:51], v[36:37], off
	s_ashr_i32 s59, s58, 31
	s_lshl_b64 s[2:3], s[58:59], 3
	s_add_u32 s2, s0, s2
	s_addc_u32 s3, s1, s3
	s_load_dwordx2 s[2:3], s[2:3], 0x0
	v_lshlrev_b32_e32 v74, 2, v166
	s_waitcnt vmcnt(23)
	v_lshlrev_b32_e32 v118, 16, v64
	v_and_b32_e32 v119, 0xffff0000, v64
	v_lshlrev_b32_e32 v122, 16, v65
	s_waitcnt lgkmcnt(0)
	v_lshl_add_u64 v[36:37], s[2:3], 0, v[84:85]
	v_lshl_add_u64 v[36:37], v[36:37], 0, v[74:75]
	v_and_b32_e32 v123, 0xffff0000, v65
	v_lshl_add_u64 v[64:65], v[36:37], 0, s[8:9]
	v_add_co_u32_e64 v36, s[2:3], s72, v36
	s_mov_b32 s28, 35
	s_nop 0
	v_addc_co_u32_e64 v37, s[2:3], 0, v37, s[2:3]
	s_waitcnt vmcnt(22)
	v_lshlrev_b32_e32 v120, 16, v80
	v_and_b32_e32 v121, 0xffff0000, v80
	v_lshlrev_b32_e32 v126, 16, v81
	v_and_b32_e32 v127, 0xffff0000, v81
	s_waitcnt vmcnt(21)
	v_lshlrev_b32_e32 v124, 16, v82
	v_and_b32_e32 v125, 0xffff0000, v82
	v_lshlrev_b32_e32 v130, 16, v83
	v_and_b32_e32 v131, 0xffff0000, v83
	s_waitcnt vmcnt(11)
	v_lshlrev_b32_e32 v80, 16, v174
	v_and_b32_e32 v81, 0xffff0000, v174
	v_lshlrev_b32_e32 v82, 16, v175
	v_and_b32_e32 v83, 0xffff0000, v175
	s_waitcnt vmcnt(10)
	v_lshlrev_b32_e32 v84, 16, v176
	v_and_b32_e32 v85, 0xffff0000, v176
	global_load_dword v169, v[36:37], off nt
	global_load_dword v174, v[64:65], off offset:256 nt
	global_load_dword v175, v[64:65], off offset:512 nt
	global_load_dword v176, v[64:65], off offset:768 nt
	s_ashr_i32 s29, s28, 31
	s_lshl_b64 s[2:3], s[28:29], 3
	s_add_u32 s2, s0, s2
	s_addc_u32 s3, s1, s3
	s_load_dwordx2 s[2:3], s[2:3], 0x0
	s_mov_b32 s34, 35
	v_lshlrev_b32_e32 v132, 16, v88
	v_and_b32_e32 v133, 0xffff0000, v88
	v_lshlrev_b32_e32 v138, 16, v89
	s_waitcnt lgkmcnt(0)
	v_lshl_add_u64 v[36:37], s[2:3], 0, v[164:165]
	v_lshl_add_u64 v[36:37], v[36:37], 0, v[74:75]
	v_lshl_add_u64 v[64:65], v[36:37], 0, s[8:9]
	v_add_co_u32_e64 v36, s[2:3], s72, v36
	v_and_b32_e32 v139, 0xffff0000, v89
	s_nop 0
	v_addc_co_u32_e64 v37, s[2:3], 0, v37, s[2:3]
	v_lshlrev_b32_e32 v140, 16, v92
	v_and_b32_e32 v141, 0xffff0000, v92
	v_lshlrev_b32_e32 v146, 16, v93
	v_and_b32_e32 v147, 0xffff0000, v93
	v_lshlrev_b32_e32 v88, 16, v177
	v_and_b32_e32 v89, 0xffff0000, v177
	s_waitcnt vmcnt(13)
	v_lshlrev_b32_e32 v92, 16, v179
	v_and_b32_e32 v93, 0xffff0000, v179
	global_load_dword v177, v[36:37], off nt
	global_load_dword v179, v[64:65], off offset:256 nt
	global_load_dword v183, v[64:65], off offset:512 nt
	global_load_dword v187, v[64:65], off offset:768 nt
	s_ashr_i32 s35, s34, 31
	s_lshl_b64 s[2:3], s[34:35], 3
	s_add_u32 s2, s0, s2
	s_addc_u32 s3, s1, s3
	s_load_dwordx2 s[2:3], s[2:3], 0x0
	s_mov_b32 s38, 35
	s_mov_b32 s44, 35
	s_mov_b32 s50, 35
	s_mov_b32 s56, 35
	s_waitcnt lgkmcnt(0)
	v_lshl_add_u64 v[36:37], s[2:3], 0, v[162:163]
	v_lshl_add_u64 v[36:37], v[36:37], 0, v[74:75]
	v_lshl_add_u64 v[64:65], v[36:37], 0, s[8:9]
	v_add_co_u32_e64 v36, s[2:3], s72, v36
	s_mov_b32 s60, 35
	s_nop 0
	v_addc_co_u32_e64 v37, s[2:3], 0, v37, s[2:3]
	global_load_dword v188, v[36:37], off nt
	global_load_dword v189, v[64:65], off offset:256 nt
	global_load_dword v190, v[64:65], off offset:512 nt
	global_load_dword v191, v[64:65], off offset:768 nt
	s_ashr_i32 s39, s38, 31
	s_lshl_b64 s[2:3], s[38:39], 3
	s_add_u32 s2, s0, s2
	s_addc_u32 s3, s1, s3
	s_load_dwordx2 s[2:3], s[2:3], 0x0
	s_mov_b32 s54, 35
	v_lshlrev_b32_e32 v128, 16, v86
	v_and_b32_e32 v129, 0xffff0000, v86
	v_lshlrev_b32_e32 v134, 16, v87
	s_waitcnt lgkmcnt(0)
	v_lshl_add_u64 v[36:37], s[2:3], 0, v[160:161]
	v_lshl_add_u64 v[36:37], v[36:37], 0, v[74:75]
	v_lshl_add_u64 v[64:65], v[36:37], 0, s[8:9]
	v_add_co_u32_e64 v36, s[2:3], s72, v36
	v_and_b32_e32 v135, 0xffff0000, v87
	s_nop 0
	v_addc_co_u32_e64 v37, s[2:3], 0, v37, s[2:3]
	global_load_dword v192, v[36:37], off nt
	global_load_dword v193, v[64:65], off offset:256 nt
	global_load_dword v194, v[64:65], off offset:512 nt
	global_load_dword v195, v[64:65], off offset:768 nt
	s_ashr_i32 s45, s44, 31
	s_lshl_b64 s[2:3], s[44:45], 3
	s_add_u32 s2, s0, s2
	s_addc_u32 s3, s1, s3
	s_load_dwordx2 s[2:3], s[2:3], 0x0
	v_lshlrev_b32_e32 v136, 16, v90
	v_and_b32_e32 v137, 0xffff0000, v90
	v_lshlrev_b32_e32 v142, 16, v91
	v_and_b32_e32 v143, 0xffff0000, v91
	s_waitcnt lgkmcnt(0)
	v_lshl_add_u64 v[36:37], s[2:3], 0, v[158:159]
	v_lshl_add_u64 v[36:37], v[36:37], 0, v[74:75]
	v_lshl_add_u64 v[64:65], v[36:37], 0, s[8:9]
	v_add_co_u32_e64 v36, s[2:3], s72, v36
	s_waitcnt vmcnt(14)
	v_cvt_f32_fp8_sdwa v160, v174 src0_sel:BYTE_2
	v_addc_co_u32_e64 v37, s[2:3], 0, v37, s[2:3]
	global_load_dword v196, v[36:37], off nt
	global_load_dword v197, v[64:65], off offset:256 nt
	global_load_dword v198, v[64:65], off offset:512 nt
	global_load_dword v199, v[64:65], off offset:768 nt
	s_ashr_i32 s51, s50, 31
	s_lshl_b64 s[2:3], s[50:51], 3
	s_add_u32 s2, s0, s2
	s_addc_u32 s3, s1, s3
	s_load_dwordx2 s[2:3], s[2:3], 0x0
	v_cvt_f32_fp8_sdwa v161, v174 src0_sel:BYTE_3
	s_waitcnt vmcnt(17)
	v_cvt_f32_fp8_e32 v162, v175
	v_cvt_f32_fp8_sdwa v163, v175 src0_sel:BYTE_1
	v_cvt_f32_fp8_sdwa v164, v175 src0_sel:BYTE_2
	s_waitcnt lgkmcnt(0)
	v_lshl_add_u64 v[64:65], s[2:3], 0, v[38:39]
	v_lshl_add_u64 v[64:65], v[64:65], 0, v[74:75]
	v_lshl_add_u64 v[158:159], v[64:65], 0, s[8:9]
	v_add_co_u32_e64 v64, s[2:3], s72, v64
	v_cvt_f32_fp8_sdwa v165, v175 src0_sel:BYTE_3
	s_nop 0
	v_addc_co_u32_e64 v65, s[2:3], 0, v65, s[2:3]
	global_load_dword v200, v[64:65], off nt
	global_load_dword v201, v[158:159], off offset:256 nt
	global_load_dword v202, v[158:159], off offset:512 nt
	global_load_dword v203, v[158:159], off offset:768 nt
	s_ashr_i32 s57, s56, 31
	s_lshl_b64 s[2:3], s[56:57], 3
	s_add_u32 s2, s0, s2
	s_addc_u32 s3, s1, s3
	s_load_dwordx2 s[2:3], s[2:3], 0x0
	v_cvt_f32_fp8_e32 v158, v174
	v_cvt_f32_fp8_sdwa v159, v174 src0_sel:BYTE_1
	v_mov_b64_e32 v[36:37], v[170:171]
	v_mov_b64_e32 v[38:39], v[172:173]
	s_waitcnt lgkmcnt(0)
	v_lshl_add_u64 v[64:65], s[2:3], 0, v[156:157]
	v_lshl_add_u64 v[64:65], v[64:65], 0, v[74:75]
	v_lshl_add_u64 v[156:157], v[64:65], 0, s[8:9]
	v_add_co_u32_e64 v64, s[2:3], s72, v64
	s_waitcnt vmcnt(20)
	v_cvt_f32_fp8_e32 v170, v176
	v_addc_co_u32_e64 v65, s[2:3], 0, v65, s[2:3]
	global_load_dword v204, v[64:65], off nt
	global_load_dword v205, v[156:157], off offset:256 nt
	global_load_dword v206, v[156:157], off offset:512 nt
	global_load_dword v207, v[156:157], off offset:768 nt
	s_ashr_i32 s61, s60, 31
	s_lshl_b64 s[2:3], s[60:61], 3
	s_add_u32 s2, s0, s2
	s_addc_u32 s3, s1, s3
	s_load_dwordx2 s[2:3], s[2:3], 0x0
	v_cvt_f32_fp8_e32 v64, v169
	v_cvt_f32_fp8_sdwa v65, v169 src0_sel:BYTE_1
	v_cvt_f32_fp8_sdwa v156, v169 src0_sel:BYTE_2
	v_cvt_f32_fp8_sdwa v157, v169 src0_sel:BYTE_3
	s_waitcnt lgkmcnt(0)
	v_lshl_add_u64 v[154:155], s[2:3], 0, v[154:155]
	v_lshl_add_u64 v[154:155], v[154:155], 0, v[74:75]
	v_lshl_add_u64 v[174:175], v[154:155], 0, s[8:9]
	v_add_co_u32_e64 v154, s[2:3], s72, v154
	v_cvt_f32_fp8_sdwa v171, v176 src0_sel:BYTE_1
	s_nop 0
	v_addc_co_u32_e64 v155, s[2:3], 0, v155, s[2:3]
	global_load_dword v169, v[154:155], off nt
	global_load_dword v208, v[174:175], off offset:256 nt
	global_load_dword v209, v[174:175], off offset:512 nt
	global_load_dword v210, v[174:175], off offset:768 nt
	s_ashr_i32 s55, s54, 31
	s_lshl_b64 s[2:3], s[54:55], 3
	s_add_u32 s2, s0, s2
	s_addc_u32 s3, s1, s3
	v_cvt_f32_fp8_sdwa v172, v176 src0_sel:BYTE_2
	v_cvt_f32_fp8_sdwa v173, v176 src0_sel:BYTE_3
	s_load_dwordx2 s[2:3], s[2:3], 0x0
	v_lshlrev_b32_e32 v144, 16, v94
	v_and_b32_e32 v145, 0xffff0000, v94
	v_lshlrev_b32_e32 v148, 16, v95
	v_and_b32_e32 v149, 0xffff0000, v95
	v_lshlrev_b32_e32 v86, 16, v178
	v_and_b32_e32 v87, 0xffff0000, v178
	v_lshlrev_b32_e32 v90, 16, v180
	v_and_b32_e32 v91, 0xffff0000, v180
	v_lshlrev_b32_e32 v94, 16, v181
	v_and_b32_e32 v95, 0xffff0000, v181
	s_waitcnt vmcnt(27)
	v_cvt_f32_fp8_e32 v154, v177
	v_cvt_f32_fp8_sdwa v155, v177 src0_sel:BYTE_1
	v_cvt_f32_fp8_sdwa v174, v177 src0_sel:BYTE_2
	v_cvt_f32_fp8_sdwa v175, v177 src0_sel:BYTE_3
	s_waitcnt vmcnt(26)
	v_cvt_f32_fp8_e32 v176, v179
	v_cvt_f32_fp8_sdwa v177, v179 src0_sel:BYTE_1
	v_cvt_f32_fp8_sdwa v178, v179 src0_sel:BYTE_2
	v_cvt_f32_fp8_sdwa v179, v179 src0_sel:BYTE_3
	s_waitcnt vmcnt(25)
	v_cvt_f32_fp8_e32 v180, v183
	v_cvt_f32_fp8_sdwa v181, v183 src0_sel:BYTE_1
	v_cvt_f32_fp8_sdwa v182, v183 src0_sel:BYTE_2
	v_cvt_f32_fp8_sdwa v183, v183 src0_sel:BYTE_3
	s_waitcnt vmcnt(24)
	v_cvt_f32_fp8_e32 v184, v187
	v_cvt_f32_fp8_sdwa v185, v187 src0_sel:BYTE_1
	v_cvt_f32_fp8_sdwa v186, v187 src0_sel:BYTE_2
	v_cvt_f32_fp8_sdwa v187, v187 src0_sel:BYTE_3
	v_pk_fma_f32 v[156:157], v[16:17], v[156:157], 0 op_sel_hi:[0,1,0]
	v_pk_fma_f32 v[64:65], v[16:17], v[64:65], 0 op_sel_hi:[0,1,0]
	v_pk_fma_f32 v[160:161], v[16:17], v[160:161], 0 op_sel_hi:[0,1,0]
	v_pk_fma_f32 v[158:159], v[16:17], v[158:159], 0 op_sel_hi:[0,1,0]
	v_pk_fma_f32 v[164:165], v[16:17], v[164:165], 0 op_sel_hi:[0,1,0]
	v_pk_fma_f32 v[162:163], v[16:17], v[162:163], 0 op_sel_hi:[0,1,0]
	v_pk_fma_f32 v[172:173], v[16:17], v[172:173], 0 op_sel_hi:[0,1,0]
	v_pk_fma_f32 v[170:171], v[16:17], v[170:171], 0 op_sel_hi:[0,1,0]
	v_pk_fma_f32 v[64:65], v[16:17], v[154:155], v[64:65] op_sel:[1,0,0]
	v_pk_fma_f32 v[154:155], v[16:17], v[174:175], v[156:157] op_sel:[1,0,0]
	v_pk_fma_f32 v[156:157], v[16:17], v[176:177], v[158:159] op_sel:[1,0,0]
	v_pk_fma_f32 v[158:159], v[16:17], v[178:179], v[160:161] op_sel:[1,0,0]
	v_pk_fma_f32 v[160:161], v[16:17], v[180:181], v[162:163] op_sel:[1,0,0]
	v_pk_fma_f32 v[162:163], v[16:17], v[182:183], v[164:165] op_sel:[1,0,0]
	v_pk_fma_f32 v[164:165], v[16:17], v[184:185], v[170:171] op_sel:[1,0,0]
	v_pk_fma_f32 v[170:171], v[16:17], v[186:187], v[172:173] op_sel:[1,0,0]
	v_mov_b64_e32 v[16:17], v[60:61]
	s_waitcnt lgkmcnt(0)
	v_lshl_add_u64 v[60:61], s[2:3], 0, v[152:153]
	v_lshl_add_u64 v[60:61], v[60:61], 0, v[74:75]
	v_lshl_add_u64 v[152:153], v[60:61], 0, s[8:9]
	v_add_co_u32_e64 v60, s[2:3], s72, v60
	s_mov_b32 s48, 35
	s_nop 0
	v_addc_co_u32_e64 v61, s[2:3], 0, v61, s[2:3]
	global_load_dword v211, v[60:61], off nt
	global_load_dword v212, v[152:153], off offset:256 nt
	global_load_dword v213, v[152:153], off offset:512 nt
	global_load_dword v214, v[152:153], off offset:768 nt
	s_ashr_i32 s49, s48, 31
	s_lshl_b64 s[2:3], s[48:49], 3
	s_add_u32 s2, s0, s2
	s_addc_u32 s3, s1, s3
	s_load_dwordx2 s[2:3], s[2:3], 0x0
	s_waitcnt vmcnt(27)
	v_cvt_f32_fp8_sdwa v152, v188 src0_sel:BYTE_2
	v_cvt_f32_fp8_sdwa v153, v188 src0_sel:BYTE_3
	s_waitcnt vmcnt(26)
	v_cvt_f32_fp8_e32 v172, v189
	v_cvt_f32_fp8_sdwa v173, v189 src0_sel:BYTE_1
	s_waitcnt vmcnt(25)
	v_cvt_f32_fp8_sdwa v178, v190 src0_sel:BYTE_2
	v_cvt_f32_fp8_sdwa v179, v190 src0_sel:BYTE_3
	s_waitcnt vmcnt(24)
	v_cvt_f32_fp8_e32 v180, v191
	v_cvt_f32_fp8_sdwa v181, v191 src0_sel:BYTE_1
	s_waitcnt lgkmcnt(0)
	v_lshl_add_u64 v[150:151], s[2:3], 0, v[150:151]
	v_lshl_add_u64 v[150:151], v[150:151], 0, v[74:75]
	v_pk_fma_f32 v[152:153], v[18:19], v[152:153], v[154:155] op_sel_hi:[0,1,1]
	v_pk_fma_f32 v[154:155], v[18:19], v[172:173], v[156:157] op_sel_hi:[0,1,1]
	v_pk_fma_f32 v[156:157], v[18:19], v[178:179], v[162:163] op_sel_hi:[0,1,1]
	v_pk_fma_f32 v[162:163], v[18:19], v[180:181], v[164:165] op_sel_hi:[0,1,1]
	v_lshl_add_u64 v[164:165], v[150:151], 0, s[8:9]
	v_add_co_u32_e64 v150, s[2:3], s72, v150
	s_mov_b32 s40, 35
	s_nop 0
	v_addc_co_u32_e64 v151, s[2:3], 0, v151, s[2:3]
	global_load_dword v215, v[150:151], off nt
	global_load_dword v216, v[164:165], off offset:256 nt
	global_load_dword v217, v[164:165], off offset:512 nt
	global_load_dword v218, v[164:165], off offset:768 nt
	s_ashr_i32 s41, s40, 31
	s_lshl_b64 s[2:3], s[40:41], 3
	s_add_u32 s2, s0, s2
	v_cvt_f32_fp8_e32 v60, v188
	v_cvt_f32_fp8_sdwa v61, v188 src0_sel:BYTE_1
	v_cvt_f32_fp8_sdwa v174, v189 src0_sel:BYTE_2
	v_cvt_f32_fp8_sdwa v175, v189 src0_sel:BYTE_3
	v_cvt_f32_fp8_e32 v176, v190
	v_cvt_f32_fp8_sdwa v177, v190 src0_sel:BYTE_1
	v_cvt_f32_fp8_sdwa v182, v191 src0_sel:BYTE_2
	v_cvt_f32_fp8_sdwa v183, v191 src0_sel:BYTE_3
	s_addc_u32 s3, s1, s3
	s_load_dwordx2 s[2:3], s[2:3], 0x0
	s_waitcnt vmcnt(27)
	v_cvt_f32_fp8_e32 v150, v192
	v_cvt_f32_fp8_sdwa v151, v192 src0_sel:BYTE_1
	v_pk_fma_f32 v[60:61], v[18:19], v[60:61], v[64:65] op_sel_hi:[0,1,1]
	v_pk_fma_f32 v[64:65], v[18:19], v[174:175], v[158:159] op_sel_hi:[0,1,1]
	v_pk_fma_f32 v[158:159], v[18:19], v[176:177], v[160:161] op_sel_hi:[0,1,1]
	v_pk_fma_f32 v[160:161], v[18:19], v[182:183], v[170:171] op_sel_hi:[0,1,1]
	v_cvt_f32_fp8_sdwa v164, v192 src0_sel:BYTE_2
	v_cvt_f32_fp8_sdwa v165, v192 src0_sel:BYTE_3
	s_waitcnt vmcnt(26)
	v_cvt_f32_fp8_e32 v170, v193
	v_cvt_f32_fp8_sdwa v171, v193 src0_sel:BYTE_1
	v_cvt_f32_fp8_sdwa v172, v193 src0_sel:BYTE_2
	v_cvt_f32_fp8_sdwa v173, v193 src0_sel:BYTE_3
	s_waitcnt vmcnt(25)
	v_cvt_f32_fp8_e32 v174, v194
	v_cvt_f32_fp8_sdwa v175, v194 src0_sel:BYTE_1
	v_cvt_f32_fp8_sdwa v176, v194 src0_sel:BYTE_2
	v_cvt_f32_fp8_sdwa v177, v194 src0_sel:BYTE_3
	s_waitcnt vmcnt(24)
	v_cvt_f32_fp8_e32 v178, v195
	v_cvt_f32_fp8_sdwa v179, v195 src0_sel:BYTE_1
	v_cvt_f32_fp8_sdwa v180, v195 src0_sel:BYTE_2
	v_cvt_f32_fp8_sdwa v181, v195 src0_sel:BYTE_3
	v_pk_fma_f32 v[150:151], v[18:19], v[150:151], v[60:61] op_sel:[1,0,0]
	s_waitcnt lgkmcnt(0)
	v_lshl_add_u64 v[60:61], s[2:3], 0, v[116:117]
	v_lshl_add_u64 v[60:61], v[60:61], 0, v[74:75]
	v_pk_fma_f32 v[152:153], v[18:19], v[164:165], v[152:153] op_sel:[1,0,0]
	v_pk_fma_f32 v[154:155], v[18:19], v[170:171], v[154:155] op_sel:[1,0,0]
	v_pk_fma_f32 v[164:165], v[18:19], v[172:173], v[64:65] op_sel:[1,0,0]
	v_pk_fma_f32 v[158:159], v[18:19], v[174:175], v[158:159] op_sel:[1,0,0]
	v_pk_fma_f32 v[156:157], v[18:19], v[176:177], v[156:157] op_sel:[1,0,0]
	v_pk_fma_f32 v[162:163], v[18:19], v[178:179], v[162:163] op_sel:[1,0,0]
	v_pk_fma_f32 v[160:161], v[18:19], v[180:181], v[160:161] op_sel:[1,0,0]
	v_mov_b64_e32 v[18:19], v[62:63]
	v_lshl_add_u64 v[62:63], v[60:61], 0, s[8:9]
	v_add_co_u32_e64 v60, s[2:3], s72, v60
	s_mov_b32 s30, 35
	s_nop 0
	v_addc_co_u32_e64 v61, s[2:3], 0, v61, s[2:3]
	global_load_dword v219, v[60:61], off nt
	global_load_dword v220, v[62:63], off offset:256 nt
	global_load_dword v221, v[62:63], off offset:512 nt
	global_load_dword v222, v[62:63], off offset:768 nt
	s_ashr_i32 s31, s30, 31
	s_lshl_b64 s[2:3], s[30:31], 3
	s_add_u32 s2, s0, s2
	s_addc_u32 s3, s1, s3
	s_load_dwordx2 s[2:3], s[2:3], 0x0
	s_mov_b32 s24, 35
	s_waitcnt vmcnt(27)
	v_cvt_f32_fp8_e32 v60, v196
	v_cvt_f32_fp8_sdwa v61, v196 src0_sel:BYTE_1
	v_cvt_f32_fp8_sdwa v62, v196 src0_sel:BYTE_2
	s_waitcnt lgkmcnt(0)
	v_lshl_add_u64 v[114:115], s[2:3], 0, v[114:115]
	v_lshl_add_u64 v[114:115], v[114:115], 0, v[74:75]
	v_lshl_add_u64 v[178:179], v[114:115], 0, s[8:9]
	v_add_co_u32_e64 v114, s[2:3], s72, v114
	v_cvt_f32_fp8_sdwa v63, v196 src0_sel:BYTE_3
	s_nop 0
	v_addc_co_u32_e64 v115, s[2:3], 0, v115, s[2:3]
	global_load_dword v223, v[114:115], off nt
	global_load_dword v224, v[178:179], off offset:256 nt
	global_load_dword v225, v[178:179], off offset:512 nt
	global_load_dword v226, v[178:179], off offset:768 nt
	s_ashr_i32 s25, s24, 31
	s_lshl_b64 s[2:3], s[24:25], 3
	s_add_u32 s2, s0, s2
	s_addc_u32 s3, s1, s3
	s_waitcnt vmcnt(30)
	v_cvt_f32_fp8_e32 v64, v197
	v_cvt_f32_fp8_sdwa v65, v197 src0_sel:BYTE_1
	v_cvt_f32_fp8_sdwa v116, v197 src0_sel:BYTE_2
	v_cvt_f32_fp8_sdwa v117, v197 src0_sel:BYTE_3
	s_waitcnt vmcnt(29)
	v_cvt_f32_fp8_e32 v170, v198
	v_cvt_f32_fp8_sdwa v171, v198 src0_sel:BYTE_1
	v_cvt_f32_fp8_sdwa v172, v198 src0_sel:BYTE_2
	v_cvt_f32_fp8_sdwa v173, v198 src0_sel:BYTE_3
	s_waitcnt vmcnt(28)
	v_cvt_f32_fp8_e32 v174, v199
	v_cvt_f32_fp8_sdwa v175, v199 src0_sel:BYTE_1
	v_cvt_f32_fp8_sdwa v176, v199 src0_sel:BYTE_2
	v_cvt_f32_fp8_sdwa v177, v199 src0_sel:BYTE_3
	s_load_dwordx2 s[2:3], s[2:3], 0x0
	s_waitcnt vmcnt(27)
	v_cvt_f32_fp8_e32 v114, v200
	v_cvt_f32_fp8_sdwa v115, v200 src0_sel:BYTE_1
	v_cvt_f32_fp8_sdwa v178, v200 src0_sel:BYTE_2
	v_cvt_f32_fp8_sdwa v179, v200 src0_sel:BYTE_3
	s_waitcnt vmcnt(26)
	v_cvt_f32_fp8_e32 v180, v201
	v_cvt_f32_fp8_sdwa v181, v201 src0_sel:BYTE_1
	v_cvt_f32_fp8_sdwa v182, v201 src0_sel:BYTE_2
	v_cvt_f32_fp8_sdwa v183, v201 src0_sel:BYTE_3
	s_waitcnt vmcnt(25)
	v_cvt_f32_fp8_e32 v184, v202
	v_cvt_f32_fp8_sdwa v185, v202 src0_sel:BYTE_1
	v_cvt_f32_fp8_sdwa v186, v202 src0_sel:BYTE_2
	v_cvt_f32_fp8_sdwa v187, v202 src0_sel:BYTE_3
	s_waitcnt vmcnt(24)
	v_cvt_f32_fp8_e32 v188, v203
	v_cvt_f32_fp8_sdwa v189, v203 src0_sel:BYTE_1
	v_cvt_f32_fp8_sdwa v190, v203 src0_sel:BYTE_2
	v_cvt_f32_fp8_sdwa v191, v203 src0_sel:BYTE_3
	v_pk_fma_f32 v[62:63], v[20:21], v[62:63], 0 op_sel_hi:[0,1,0]
	v_pk_fma_f32 v[60:61], v[20:21], v[60:61], 0 op_sel_hi:[0,1,0]
	v_pk_fma_f32 v[116:117], v[20:21], v[116:117], 0 op_sel_hi:[0,1,0]
	v_pk_fma_f32 v[64:65], v[20:21], v[64:65], 0 op_sel_hi:[0,1,0]
	v_pk_fma_f32 v[172:173], v[20:21], v[172:173], 0 op_sel_hi:[0,1,0]
	v_pk_fma_f32 v[170:171], v[20:21], v[170:171], 0 op_sel_hi:[0,1,0]
	v_pk_fma_f32 v[176:177], v[20:21], v[176:177], 0 op_sel_hi:[0,1,0]
	v_pk_fma_f32 v[174:175], v[20:21], v[174:175], 0 op_sel_hi:[0,1,0]
	v_pk_fma_f32 v[60:61], v[20:21], v[114:115], v[60:61] op_sel:[1,0,0]
	v_pk_fma_f32 v[62:63], v[20:21], v[178:179], v[62:63] op_sel:[1,0,0]
	v_pk_fma_f32 v[64:65], v[20:21], v[180:181], v[64:65] op_sel:[1,0,0]
	v_pk_fma_f32 v[114:115], v[20:21], v[182:183], v[116:117] op_sel:[1,0,0]
	v_pk_fma_f32 v[116:117], v[20:21], v[184:185], v[170:171] op_sel:[1,0,0]
	v_pk_fma_f32 v[170:171], v[20:21], v[186:187], v[172:173] op_sel:[1,0,0]
	v_pk_fma_f32 v[172:173], v[20:21], v[188:189], v[174:175] op_sel:[1,0,0]
	v_pk_fma_f32 v[174:175], v[20:21], v[190:191], v[176:177] op_sel:[1,0,0]
	v_mov_b64_e32 v[20:21], v[56:57]
	s_waitcnt lgkmcnt(0)
	v_lshl_add_u64 v[56:57], s[2:3], 0, v[70:71]
	v_lshl_add_u64 v[56:57], v[56:57], 0, v[74:75]
	v_lshl_add_u64 v[70:71], v[56:57], 0, s[8:9]
	v_add_co_u32_e64 v56, s[2:3], s72, v56
	s_mov_b32 s20, 35
	s_nop 0
	v_addc_co_u32_e64 v57, s[2:3], 0, v57, s[2:3]
	global_load_dword v200, v[56:57], off nt
	global_load_dword v201, v[70:71], off offset:256 nt
	global_load_dword v202, v[70:71], off offset:512 nt
	global_load_dword v203, v[70:71], off offset:768 nt
	s_ashr_i32 s21, s20, 31
	s_lshl_b64 s[2:3], s[20:21], 3
	s_add_u32 s2, s0, s2
	s_addc_u32 s3, s1, s3
	s_load_dwordx2 s[2:3], s[2:3], 0x0
	s_waitcnt vmcnt(27)
	v_cvt_f32_fp8_sdwa v70, v204 src0_sel:BYTE_2
	v_cvt_f32_fp8_sdwa v71, v204 src0_sel:BYTE_3
	s_waitcnt vmcnt(25)
	v_cvt_f32_fp8_sdwa v182, v206 src0_sel:BYTE_2
	v_cvt_f32_fp8_sdwa v183, v206 src0_sel:BYTE_3
	s_waitcnt vmcnt(24)
	v_cvt_f32_fp8_e32 v184, v207
	v_cvt_f32_fp8_sdwa v185, v207 src0_sel:BYTE_1
	s_waitcnt lgkmcnt(0)
	v_lshl_add_u64 v[68:69], s[2:3], 0, v[68:69]
	v_lshl_add_u64 v[68:69], v[68:69], 0, v[74:75]
	v_pk_fma_f32 v[62:63], v[22:23], v[70:71], v[62:63] op_sel_hi:[0,1,1]
	v_pk_fma_f32 v[70:71], v[22:23], v[182:183], v[170:171] op_sel_hi:[0,1,1]
	v_pk_fma_f32 v[170:171], v[22:23], v[184:185], v[172:173] op_sel_hi:[0,1,1]
	v_lshl_add_u64 v[172:173], v[68:69], 0, s[8:9]
	v_add_co_u32_e64 v68, s[2:3], s72, v68
	s_mov_b32 s16, 35
	s_nop 0
	v_addc_co_u32_e64 v69, s[2:3], 0, v69, s[2:3]
	v_cvt_f32_fp8_e32 v56, v204
	v_cvt_f32_fp8_sdwa v57, v204 src0_sel:BYTE_1
	v_cvt_f32_fp8_e32 v176, v205
	v_cvt_f32_fp8_sdwa v177, v205 src0_sel:BYTE_1
	v_cvt_f32_fp8_sdwa v178, v205 src0_sel:BYTE_2
	v_cvt_f32_fp8_sdwa v179, v205 src0_sel:BYTE_3
	v_cvt_f32_fp8_e32 v180, v206
	v_cvt_f32_fp8_sdwa v181, v206 src0_sel:BYTE_1
	v_cvt_f32_fp8_sdwa v186, v207 src0_sel:BYTE_2
	v_cvt_f32_fp8_sdwa v187, v207 src0_sel:BYTE_3
	global_load_dword v204, v[68:69], off nt
	global_load_dword v205, v[172:173], off offset:256 nt
	global_load_dword v206, v[172:173], off offset:512 nt
	global_load_dword v207, v[172:173], off offset:768 nt
	s_ashr_i32 s17, s16, 31
	s_lshl_b64 s[2:3], s[16:17], 3
	s_add_u32 s2, s0, s2
	s_addc_u32 s3, s1, s3
	s_load_dwordx2 s[2:3], s[2:3], 0x0
	s_waitcnt vmcnt(27)
	v_cvt_f32_fp8_e32 v68, v169
	v_cvt_f32_fp8_sdwa v69, v169 src0_sel:BYTE_1
	v_pk_fma_f32 v[56:57], v[22:23], v[56:57], v[60:61] op_sel_hi:[0,1,1]
	v_pk_fma_f32 v[60:61], v[22:23], v[178:179], v[114:115] op_sel_hi:[0,1,1]
	v_pk_fma_f32 v[64:65], v[22:23], v[176:177], v[64:65] op_sel_hi:[0,1,1]
	v_pk_fma_f32 v[114:115], v[22:23], v[180:181], v[116:117] op_sel_hi:[0,1,1]
	v_pk_fma_f32 v[116:117], v[22:23], v[186:187], v[174:175] op_sel_hi:[0,1,1]
	v_cvt_f32_fp8_sdwa v172, v169 src0_sel:BYTE_2
	v_cvt_f32_fp8_sdwa v173, v169 src0_sel:BYTE_3
	s_waitcnt vmcnt(26)
	v_cvt_f32_fp8_e32 v174, v208
	v_cvt_f32_fp8_sdwa v175, v208 src0_sel:BYTE_1
	v_cvt_f32_fp8_sdwa v176, v208 src0_sel:BYTE_2
	v_cvt_f32_fp8_sdwa v177, v208 src0_sel:BYTE_3
	s_waitcnt vmcnt(25)
	v_cvt_f32_fp8_e32 v178, v209
	v_cvt_f32_fp8_sdwa v179, v209 src0_sel:BYTE_1
	v_cvt_f32_fp8_sdwa v180, v209 src0_sel:BYTE_2
	v_cvt_f32_fp8_sdwa v181, v209 src0_sel:BYTE_3
	s_waitcnt vmcnt(24)
	v_cvt_f32_fp8_e32 v182, v210
	v_cvt_f32_fp8_sdwa v183, v210 src0_sel:BYTE_1
	v_cvt_f32_fp8_sdwa v184, v210 src0_sel:BYTE_2
	v_cvt_f32_fp8_sdwa v185, v210 src0_sel:BYTE_3
	v_pk_fma_f32 v[186:187], v[22:23], v[68:69], v[56:57] op_sel:[1,0,0]
	s_waitcnt lgkmcnt(0)
	v_lshl_add_u64 v[56:57], s[2:3], 0, v[66:67]
	v_lshl_add_u64 v[56:57], v[56:57], 0, v[74:75]
	v_pk_fma_f32 v[172:173], v[22:23], v[172:173], v[62:63] op_sel:[1,0,0]
	v_pk_fma_f32 v[174:175], v[22:23], v[174:175], v[64:65] op_sel:[1,0,0]
	v_pk_fma_f32 v[176:177], v[22:23], v[176:177], v[60:61] op_sel:[1,0,0]
	v_pk_fma_f32 v[178:179], v[22:23], v[178:179], v[114:115] op_sel:[1,0,0]
	v_pk_fma_f32 v[180:181], v[22:23], v[180:181], v[70:71] op_sel:[1,0,0]
	v_pk_fma_f32 v[170:171], v[22:23], v[182:183], v[170:171] op_sel:[1,0,0]
	v_pk_fma_f32 v[182:183], v[22:23], v[184:185], v[116:117] op_sel:[1,0,0]
	v_mov_b64_e32 v[22:23], v[58:59]
	v_lshl_add_u64 v[58:59], v[56:57], 0, s[8:9]
	v_add_co_u32_e64 v56, s[2:3], s72, v56
	s_mov_b32 s12, 35
	s_nop 0
	v_addc_co_u32_e64 v57, s[2:3], 0, v57, s[2:3]
	global_load_dword v208, v[56:57], off nt
	global_load_dword v209, v[58:59], off offset:256 nt
	global_load_dword v210, v[58:59], off offset:512 nt
	global_load_dword v227, v[58:59], off offset:768 nt
	ds_read_b128 v[68:71], v168
	ds_read_b128 v[64:67], v168 offset:1024
	ds_read_b128 v[60:63], v168 offset:2048
	ds_read_b128 v[56:59], v168 offset:3072
	s_ashr_i32 s13, s12, 31
	s_lshl_b64 s[2:3], s[12:13], 3
	s_waitcnt vmcnt(27)
	v_cvt_f32_fp8_e32 v168, v211
	v_cvt_f32_fp8_sdwa v169, v211 src0_sel:BYTE_1
	s_add_u32 s2, s0, s2
	s_waitcnt vmcnt(26)
	v_cvt_f32_fp8_e32 v188, v212
	v_cvt_f32_fp8_sdwa v189, v212 src0_sel:BYTE_1
	v_cvt_f32_fp8_sdwa v190, v212 src0_sel:BYTE_2
	v_cvt_f32_fp8_sdwa v191, v212 src0_sel:BYTE_3
	s_waitcnt vmcnt(25)
	v_cvt_f32_fp8_e32 v192, v213
	v_cvt_f32_fp8_sdwa v193, v213 src0_sel:BYTE_1
	s_addc_u32 s3, s1, s3
	s_load_dwordx2 s[2:3], s[2:3], 0x0
	v_cvt_f32_fp8_sdwa v194, v213 src0_sel:BYTE_2
	v_cvt_f32_fp8_sdwa v195, v213 src0_sel:BYTE_3
	s_waitcnt lgkmcnt(0)
	v_pk_fma_f32 v[152:153], v[70:71], v[152:153], v[122:123]
	v_pk_fma_f32 v[150:151], v[68:69], v[150:151], v[118:119]
	v_pk_fma_f32 v[164:165], v[66:67], v[164:165], v[126:127]
	v_pk_fma_f32 v[154:155], v[64:65], v[154:155], v[120:121]
	v_pk_fma_f32 v[130:131], v[62:63], v[156:157], v[130:131]
	v_pk_fma_f32 v[156:157], v[60:61], v[158:159], v[124:125]
	v_pk_fma_f32 v[158:159], v[56:57], v[162:163], v[128:129]
	v_pk_fma_f32 v[120:121], v[70:71], v[172:173], v[138:139]
	v_pk_fma_f32 v[128:129], v[68:69], v[186:187], v[132:133]
	v_pk_fma_f32 v[114:115], v[66:67], v[176:177], v[142:143]
	v_pk_fma_f32 v[122:123], v[64:65], v[174:175], v[136:137]
	v_pk_fma_f32 v[134:135], v[58:59], v[160:161], v[134:135]
	v_pk_fma_f32 v[116:117], v[62:63], v[180:181], v[146:147]
	v_pk_fma_f32 v[124:125], v[60:61], v[178:179], v[140:141]
	v_pk_fma_f32 v[118:119], v[58:59], v[182:183], v[148:149]
	v_pk_fma_f32 v[126:127], v[56:57], v[170:171], v[144:145]
	v_pk_fma_f32 v[136:137], v[24:25], v[168:169], 0 op_sel_hi:[0,1,0]
	v_pk_mul_f32 v[160:161], v[150:151], v[150:151]
	v_pk_mul_f32 v[162:163], v[152:153], v[152:153]
	v_pk_mul_f32 v[168:169], v[154:155], v[154:155]
	v_pk_mul_f32 v[170:171], v[164:165], v[164:165]
	v_mul_f32_e32 v172, v157, v157
	v_mul_f32_e32 v174, v131, v131
	v_pk_mul_f32 v[176:177], v[128:129], v[128:129]
	v_pk_mul_f32 v[178:179], v[120:121], v[120:121]
	v_pk_mul_f32 v[180:181], v[122:123], v[122:123]
	v_pk_mul_f32 v[182:183], v[114:115], v[114:115]
	v_pk_fma_f32 v[138:139], v[24:25], v[190:191], 0 op_sel_hi:[0,1,0]
	v_pk_fma_f32 v[140:141], v[24:25], v[188:189], 0 op_sel_hi:[0,1,0]
	v_pk_fma_f32 v[144:145], v[24:25], v[192:193], 0 op_sel_hi:[0,1,0]
	v_mul_f32_e32 v191, v134, v134
	v_mul_f32_e32 v192, v135, v135
	v_pk_mov_b32 v[188:189], v[160:161], v[162:163] op_sel:[1,0]
	v_mov_b32_e32 v161, v163
	v_pk_mov_b32 v[162:163], v[168:169], v[170:171] op_sel:[1,0]
	v_mov_b32_e32 v169, v171
	v_pk_fma_f32 v[170:171], v[156:157], v[156:157], v[172:173] op_sel_hi:[1,1,0]
	v_pk_fma_f32 v[172:173], v[130:131], v[130:131], v[174:175] op_sel_hi:[1,1,0]
	v_pk_mov_b32 v[174:175], v[176:177], v[178:179] op_sel:[1,0]
	v_mov_b32_e32 v177, v179
	v_pk_mov_b32 v[178:179], v[180:181], v[182:183] op_sel:[1,0]
	v_mov_b32_e32 v181, v183
	v_pk_add_f32 v[160:161], v[188:189], v[160:161]
	v_pk_add_f32 v[162:163], v[162:163], v[168:169]
	v_mov_b32_e32 v171, v191
	v_mov_b32_e32 v173, v192
	v_pk_add_f32 v[168:169], v[174:175], v[176:177]
	v_pk_add_f32 v[174:175], v[178:179], v[180:181]
	v_pk_fma_f32 v[142:143], v[24:25], v[194:195], 0 op_sel_hi:[0,1,0]
	v_mul_f32_e32 v187, v158, v158
	v_mul_f32_e32 v190, v159, v159
	v_mul_f32_e32 v193, v126, v126
	v_mul_f32_e32 v194, v127, v127
	v_pk_add_f32 v[160:161], v[160:161], v[160:161] op_sel:[0,1] op_sel_hi:[1,0]
	v_pk_add_f32 v[162:163], v[162:163], v[162:163] op_sel:[0,1] op_sel_hi:[1,0]
	v_pk_add_f32 v[170:171], v[170:171], v[172:173]
	v_pk_add_f32 v[168:169], v[168:169], v[168:169] op_sel:[0,1] op_sel_hi:[1,0]
	v_pk_add_f32 v[172:173], v[174:175], v[174:175] op_sel:[0,1] op_sel_hi:[1,0]
	v_lshl_add_u64 v[96:97], s[2:3], 0, v[96:97]
	v_mov_b32_e32 v161, v187
	v_mov_b32_e32 v163, v190
	v_mov_b32_e32 v169, v193
	v_mov_b32_e32 v173, v194
	v_lshl_add_u64 v[96:97], v[96:97], 0, v[74:75]
	v_pk_add_f32 v[160:161], v[160:161], v[162:163]
	v_pk_add_f32 v[162:163], v[168:169], v[172:173]
	v_lshl_add_u64 v[168:169], v[96:97], 0, s[8:9]
	v_add_co_u32_e64 v96, s[2:3], s72, v96
	v_cvt_f32_fp8_sdwa v184, v211 src0_sel:BYTE_2
	s_nop 0
	v_addc_co_u32_e64 v97, s[2:3], 0, v97, s[2:3]
	global_load_dword v178, v[96:97], off nt
	global_load_dword v179, v[168:169], off offset:256 nt
	global_load_dword v180, v[168:169], off offset:512 nt
	global_load_dword v181, v[168:169], off offset:768 nt
	v_cvt_f32_fp8_sdwa v185, v211 src0_sel:BYTE_3
	s_waitcnt vmcnt(28)
	v_cvt_f32_fp8_e32 v196, v214
	v_cvt_f32_fp8_sdwa v197, v214 src0_sel:BYTE_1
	v_pk_add_f32 v[160:161], v[160:161], v[170:171]
	v_pk_fma_f32 v[132:133], v[24:25], v[184:185], 0 op_sel_hi:[0,1,0]
	v_mul_f32_e32 v184, v125, v125
	v_mul_f32_e32 v186, v117, v117
	v_add_f32_e32 v74, v160, v161
	v_pk_fma_f32 v[148:149], v[24:25], v[196:197], 0 op_sel_hi:[0,1,0]
	v_mul_f32_e32 v195, v118, v118
	v_mul_f32_e32 v196, v119, v119
	v_pk_fma_f32 v[182:183], v[124:125], v[124:125], v[184:185] op_sel_hi:[1,1,0]
	v_pk_fma_f32 v[184:185], v[116:117], v[116:117], v[186:187] op_sel_hi:[1,1,0]
	v_add_f32_dpp v74, v74, v74 quad_perm:[1,0,3,2] row_mask:0xf bank_mask:0xf bound_ctrl:1
	v_mov_b32_e32 v183, v195
	v_mov_b32_e32 v185, v196
	v_add_f32_dpp v74, v74, v74 quad_perm:[2,3,0,1] row_mask:0xf bank_mask:0xf bound_ctrl:1
	v_pk_add_f32 v[174:175], v[182:183], v[184:185]
	v_mbcnt_lo_u32_b32 v96, -1, 0
	v_mbcnt_hi_u32_b32 v96, -1, v96
	v_cvt_f32_fp8_sdwa v198, v214 src0_sel:BYTE_2
	v_lshlrev_b32_e32 v182, 2, v96
	v_add_f32_dpp v74, v74, v74 row_half_mirror row_mask:0xf bank_mask:0xf bound_ctrl:1
	v_pk_add_f32 v[162:163], v[162:163], v[174:175]
	v_xor_b32_e32 v182, 64, v182
	v_add_f32_dpp v74, v74, v74 row_mirror row_mask:0xf bank_mask:0xf bound_ctrl:1
	v_cvt_f32_fp8_sdwa v199, v214 src0_sel:BYTE_3
	v_add_f32_e32 v97, v162, v163
	ds_bpermute_b32 v182, v182, v74
	s_waitcnt vmcnt(27)
	v_cvt_f32_fp8_e32 v96, v215
	v_add_f32_dpp v183, v97, v97 quad_perm:[1,0,3,2] row_mask:0xf bank_mask:0xf bound_ctrl:1
	v_cvt_f32_fp8_sdwa v97, v215 src0_sel:BYTE_1
	v_cvt_f32_fp8_sdwa v160, v215 src0_sel:BYTE_2
	v_cvt_f32_fp8_sdwa v161, v215 src0_sel:BYTE_3
	s_waitcnt vmcnt(26)
	v_cvt_f32_fp8_e32 v162, v216
	v_cvt_f32_fp8_sdwa v163, v216 src0_sel:BYTE_1
	v_cvt_f32_fp8_sdwa v168, v216 src0_sel:BYTE_2
	v_cvt_f32_fp8_sdwa v169, v216 src0_sel:BYTE_3
	s_waitcnt vmcnt(25)
	v_cvt_f32_fp8_e32 v170, v217
	v_cvt_f32_fp8_sdwa v171, v217 src0_sel:BYTE_1
	v_cvt_f32_fp8_sdwa v172, v217 src0_sel:BYTE_2
	v_cvt_f32_fp8_sdwa v173, v217 src0_sel:BYTE_3
	s_waitcnt vmcnt(24)
	v_cvt_f32_fp8_e32 v174, v218
	v_cvt_f32_fp8_sdwa v175, v218 src0_sel:BYTE_1
	v_cvt_f32_fp8_sdwa v176, v218 src0_sel:BYTE_2
	v_cvt_f32_fp8_sdwa v177, v218 src0_sel:BYTE_3
	v_pk_fma_f32 v[146:147], v[24:25], v[198:199], 0 op_sel_hi:[0,1,0]
	v_pk_fma_f32 v[96:97], v[24:25], v[96:97], v[136:137] op_sel:[1,0,0]
	v_pk_fma_f32 v[132:133], v[24:25], v[160:161], v[132:133] op_sel:[1,0,0]
	v_pk_fma_f32 v[136:137], v[24:25], v[162:163], v[140:141] op_sel:[1,0,0]
	v_pk_fma_f32 v[138:139], v[24:25], v[168:169], v[138:139] op_sel:[1,0,0]
	v_pk_fma_f32 v[140:141], v[24:25], v[170:171], v[144:145] op_sel:[1,0,0]
	v_pk_fma_f32 v[142:143], v[24:25], v[172:173], v[142:143] op_sel:[1,0,0]
	v_pk_fma_f32 v[144:145], v[24:25], v[174:175], v[148:149] op_sel:[1,0,0]
	v_pk_fma_f32 v[146:147], v[24:25], v[176:177], v[146:147] op_sel:[1,0,0]
	v_mov_b64_e32 v[24:25], v[52:53]
	s_waitcnt lgkmcnt(0)
	v_add_f32_e32 v52, v74, v182
	v_mov_b32_e32 v53, v52
	s_mov_b32 s66, 34
	s_nop 1
	v_permlane32_swap_b32 v52, v53
	s_ashr_i32 s67, s66, 31
	v_add_f32_e32 v52, v52, v53
	v_fmamk_f32 v74, v52, 0x3a800000, v73
	s_lshl_b64 s[10:11], s[66:67], 3
	v_mul_f32_e32 v176, 0x4b800000, v74
	s_add_u32 s10, s0, s10
	v_cmp_gt_f32_e64 s[2:3], s74, v74
	s_addc_u32 s11, s1, s11
	s_waitcnt vmcnt(23)
	v_cvt_f32_fp8_sdwa v148, v219 src0_sel:BYTE_2
	v_cndmask_b32_e64 v74, v74, v176, s[2:3]
	v_cvt_f32_fp8_sdwa v149, v219 src0_sel:BYTE_3
	v_rsq_f32_e32 v74, v74
	s_load_dwordx2 s[10:11], s[10:11], 0x0
	v_cvt_f32_fp8_e32 v52, v219
	v_cvt_f32_fp8_sdwa v53, v219 src0_sel:BYTE_1
	s_waitcnt vmcnt(22)
	v_cvt_f32_fp8_e32 v160, v220
	v_cvt_f32_fp8_sdwa v161, v220 src0_sel:BYTE_1
	v_cvt_f32_fp8_sdwa v162, v220 src0_sel:BYTE_2
	v_cvt_f32_fp8_sdwa v163, v220 src0_sel:BYTE_3
	s_waitcnt vmcnt(21)
	v_cvt_f32_fp8_e32 v168, v221
	v_cvt_f32_fp8_sdwa v169, v221 src0_sel:BYTE_1
	v_cvt_f32_fp8_sdwa v170, v221 src0_sel:BYTE_2
	v_cvt_f32_fp8_sdwa v171, v221 src0_sel:BYTE_3
	s_waitcnt vmcnt(20)
	v_cvt_f32_fp8_e32 v172, v222
	v_cvt_f32_fp8_sdwa v173, v222 src0_sel:BYTE_1
	v_pk_fma_f32 v[148:149], v[26:27], v[148:149], v[132:133] op_sel_hi:[0,1,1]
	v_mul_f32_e32 v132, 0x45800000, v74
	v_cndmask_b32_e64 v74, v74, v132, s[2:3]
	s_waitcnt lgkmcnt(0)
	v_lshl_add_u64 v[132:133], s[10:11], 0, v[78:79]
	v_pk_fma_f32 v[52:53], v[26:27], v[52:53], v[96:97] op_sel_hi:[0,1,1]
	v_pk_fma_f32 v[96:97], v[26:27], v[162:163], v[138:139] op_sel_hi:[0,1,1]
	v_pk_fma_f32 v[160:161], v[26:27], v[160:161], v[136:137] op_sel_hi:[0,1,1]
	v_pk_mul_f32 v[136:137], v[150:151], v[74:75] op_sel_hi:[1,0]
	v_pk_mul_f32 v[138:139], v[152:153], v[74:75] op_sel_hi:[1,0]
	v_add_co_u32_e64 v150, s[2:3], s75, v132
	v_pk_fma_f32 v[162:163], v[26:27], v[170:171], v[142:143] op_sel_hi:[0,1,1]
	v_pk_fma_f32 v[168:169], v[26:27], v[168:169], v[140:141] op_sel_hi:[0,1,1]
	v_pk_fma_f32 v[170:171], v[26:27], v[172:173], v[144:145] op_sel_hi:[0,1,1]
	v_addc_co_u32_e64 v151, s[2:3], -1, v133, s[2:3]
	v_pk_mul_f32 v[140:141], v[154:155], v[74:75] op_sel_hi:[1,0]
	v_pk_mul_f32 v[142:143], v[164:165], v[74:75] op_sel_hi:[1,0]
	v_pk_mul_f32 v[144:145], v[156:157], v[74:75] op_sel_hi:[1,0]
	v_pk_mul_f32 v[152:153], v[130:131], v[74:75] op_sel_hi:[1,0]
	v_pk_mul_f32 v[154:155], v[158:159], v[74:75] op_sel_hi:[1,0]
	v_pk_mul_f32 v[156:157], v[134:135], v[74:75] op_sel_hi:[1,0]
	v_pk_mul_f32 v[132:133], v[2:3], v[138:139]
	v_pk_mul_f32 v[130:131], v[0:1], v[136:137]
	v_add_f32_dpp v183, v183, v183 quad_perm:[2,3,0,1] row_mask:0xf bank_mask:0xf bound_ctrl:1
	v_pk_mul_f32 v[136:137], v[6:7], v[142:143]
	v_pk_mul_f32 v[134:135], v[4:5], v[140:141]
	v_pk_mul_f32 v[140:141], v[10:11], v[152:153]
	v_pk_mul_f32 v[138:139], v[8:9], v[144:145]
	v_pk_mul_f32 v[144:145], v[14:15], v[156:157]
	v_pk_mul_f32 v[142:143], v[12:13], v[154:155]
	global_store_dwordx4 v[150:151], v[130:133], off offset:-3072
	global_store_dwordx4 v[150:151], v[134:137], off offset:-2048
	global_store_dwordx4 v[150:151], v[138:141], off offset:-1024
	global_store_dwordx4 v[150:151], v[142:145], off
	v_mbcnt_lo_u32_b32 v74, -1, 0
	v_mbcnt_hi_u32_b32 v74, -1, v74
	v_add_f32_dpp v183, v183, v183 row_half_mirror row_mask:0xf bank_mask:0xf bound_ctrl:1
	v_lshlrev_b32_e32 v74, 2, v74
	v_xor_b32_e32 v74, 64, v74
	v_add_f32_dpp v183, v183, v183 row_mirror row_mask:0xf bank_mask:0xf bound_ctrl:1
	v_cvt_f32_fp8_sdwa v174, v222 src0_sel:BYTE_2
	v_cvt_f32_fp8_sdwa v175, v222 src0_sel:BYTE_3
	s_waitcnt vmcnt(23)
	v_cvt_f32_fp8_e32 v130, v223
	v_cvt_f32_fp8_sdwa v131, v223 src0_sel:BYTE_1
	v_cvt_f32_fp8_sdwa v132, v223 src0_sel:BYTE_2
	v_cvt_f32_fp8_sdwa v133, v223 src0_sel:BYTE_3
	s_waitcnt vmcnt(22)
	v_cvt_f32_fp8_e32 v134, v224
	v_cvt_f32_fp8_sdwa v135, v224 src0_sel:BYTE_1
	v_cvt_f32_fp8_sdwa v136, v224 src0_sel:BYTE_2
	v_cvt_f32_fp8_sdwa v137, v224 src0_sel:BYTE_3
	s_waitcnt vmcnt(21)
	v_cvt_f32_fp8_e32 v138, v225
	v_cvt_f32_fp8_sdwa v139, v225 src0_sel:BYTE_1
	v_cvt_f32_fp8_sdwa v140, v225 src0_sel:BYTE_2
	v_cvt_f32_fp8_sdwa v141, v225 src0_sel:BYTE_3
	ds_bpermute_b32 v74, v74, v183
	s_waitcnt vmcnt(20)
	v_cvt_f32_fp8_e32 v142, v226
	v_cvt_f32_fp8_sdwa v143, v226 src0_sel:BYTE_1
	v_cvt_f32_fp8_sdwa v144, v226 src0_sel:BYTE_2
	v_cvt_f32_fp8_sdwa v145, v226 src0_sel:BYTE_3
	v_lshlrev_b32_e32 v98, 16, v100
	v_and_b32_e32 v99, 0xffff0000, v100
	v_lshlrev_b32_e32 v102, 16, v101
	v_and_b32_e32 v103, 0xffff0000, v101
	v_lshlrev_b32_e32 v100, 16, v104
	v_and_b32_e32 v101, 0xffff0000, v104
	v_lshlrev_b32_e32 v106, 16, v105
	v_and_b32_e32 v107, 0xffff0000, v105
	v_lshlrev_b32_e32 v104, 16, v108
	v_and_b32_e32 v105, 0xffff0000, v108
	v_lshlrev_b32_e32 v110, 16, v109
	v_and_b32_e32 v111, 0xffff0000, v109
	v_pk_fma_f32 v[146:147], v[26:27], v[174:175], v[146:147] op_sel_hi:[0,1,1]
	v_pk_fma_f32 v[52:53], v[26:27], v[130:131], v[52:53] op_sel:[1,0,0]
	v_pk_fma_f32 v[130:131], v[26:27], v[132:133], v[148:149] op_sel:[1,0,0]
	v_pk_fma_f32 v[132:133], v[26:27], v[134:135], v[160:161] op_sel:[1,0,0]
	v_pk_fma_f32 v[96:97], v[26:27], v[136:137], v[96:97] op_sel:[1,0,0]
	v_pk_fma_f32 v[134:135], v[26:27], v[138:139], v[168:169] op_sel:[1,0,0]
	v_pk_fma_f32 v[136:137], v[26:27], v[140:141], v[162:163] op_sel:[1,0,0]
	v_lshlrev_b32_e32 v108, 16, v112
	v_and_b32_e32 v109, 0xffff0000, v112
	v_lshlrev_b32_e32 v112, 16, v113
	v_and_b32_e32 v113, 0xffff0000, v113
	v_pk_fma_f32 v[138:139], v[26:27], v[142:143], v[170:171] op_sel:[1,0,0]
	v_pk_fma_f32 v[140:141], v[26:27], v[144:145], v[146:147] op_sel:[1,0,0]
	v_pk_fma_f32 v[130:131], v[70:71], v[130:131], v[102:103]
	v_pk_fma_f32 v[142:143], v[68:69], v[52:53], v[98:99]
	v_pk_fma_f32 v[144:145], v[66:67], v[96:97], v[106:107]
	v_pk_fma_f32 v[132:133], v[64:65], v[132:133], v[100:101]
	v_pk_fma_f32 v[110:111], v[62:63], v[136:137], v[110:111]
	v_pk_fma_f32 v[134:135], v[60:61], v[134:135], v[104:105]
	s_waitcnt lgkmcnt(0)
	v_add_f32_e32 v104, v183, v74
	s_mov_b32 s64, 34
	v_mov_b64_e32 v[26:27], v[54:55]
	v_pk_fma_f32 v[112:113], v[58:59], v[140:141], v[112:113]
	v_mov_b32_e32 v105, v104
	v_pk_mul_f32 v[52:53], v[142:143], v[142:143]
	v_pk_mul_f32 v[54:55], v[130:131], v[130:131]
	v_pk_mul_f32 v[96:97], v[132:133], v[132:133]
	v_pk_mul_f32 v[98:99], v[144:145], v[144:145]
	v_mul_f32_e32 v74, v135, v135
	v_mul_f32_e32 v100, v111, v111
	v_mul_f32_e32 v136, v112, v112
	v_mul_f32_e32 v137, v113, v113
	s_nop 1
	v_permlane32_swap_b32 v104, v105
	v_pk_mov_b32 v[102:103], v[52:53], v[54:55] op_sel:[1,0]
	v_mov_b32_e32 v53, v55
	v_pk_mov_b32 v[54:55], v[96:97], v[98:99] op_sel:[1,0]
	v_mov_b32_e32 v97, v99
	v_pk_fma_f32 v[98:99], v[134:135], v[134:135], v[74:75] op_sel_hi:[1,1,0]
	v_pk_fma_f32 v[100:101], v[110:111], v[110:111], v[100:101] op_sel_hi:[1,1,0]
	v_add_f32_e32 v74, v104, v105
	s_ashr_i32 s65, s64, 31
	v_pk_fma_f32 v[108:109], v[56:57], v[138:139], v[108:109]
	v_pk_add_f32 v[52:53], v[102:103], v[52:53]
	v_pk_add_f32 v[54:55], v[54:55], v[96:97]
	v_mov_b32_e32 v99, v136
	v_mov_b32_e32 v101, v137
	v_fmamk_f32 v74, v74, 0x3a800000, v73
	s_lshl_b64 s[10:11], s[64:65], 3
	v_mul_f32_e32 v106, v108, v108
	v_mul_f32_e32 v107, v109, v109
	v_pk_add_f32 v[52:53], v[52:53], v[52:53] op_sel:[0,1] op_sel_hi:[1,0]
	v_pk_add_f32 v[54:55], v[54:55], v[54:55] op_sel:[0,1] op_sel_hi:[1,0]
	v_pk_add_f32 v[96:97], v[98:99], v[100:101]
	v_mul_f32_e32 v98, 0x4b800000, v74
	s_add_u32 s10, s0, s10
	v_cmp_gt_f32_e64 s[2:3], s74, v74
	v_mov_b32_e32 v53, v106
	v_mov_b32_e32 v55, v107
	v_cndmask_b32_e64 v74, v74, v98, s[2:3]
	s_addc_u32 s11, s1, s11
	v_pk_add_f32 v[52:53], v[52:53], v[54:55]
	v_rsq_f32_e32 v74, v74
	s_load_dwordx2 s[10:11], s[10:11], 0x0
	v_pk_add_f32 v[52:53], v[52:53], v[96:97]
	s_waitcnt vmcnt(19)
	v_cvt_f32_fp8_e32 v54, v200
	v_cvt_f32_fp8_sdwa v55, v200 src0_sel:BYTE_1
	v_cvt_f32_fp8_sdwa v96, v200 src0_sel:BYTE_2
	v_cvt_f32_fp8_sdwa v97, v200 src0_sel:BYTE_3
	s_waitcnt vmcnt(18)
	v_cvt_f32_fp8_e32 v98, v201
	v_cvt_f32_fp8_sdwa v99, v201 src0_sel:BYTE_1
	v_add_f32_e32 v52, v52, v53
	v_cvt_f32_fp8_sdwa v100, v201 src0_sel:BYTE_2
	v_cvt_f32_fp8_sdwa v101, v201 src0_sel:BYTE_3
	s_waitcnt vmcnt(17)
	v_cvt_f32_fp8_e32 v102, v202
	v_cvt_f32_fp8_sdwa v103, v202 src0_sel:BYTE_1
	v_cvt_f32_fp8_sdwa v104, v202 src0_sel:BYTE_2
	v_cvt_f32_fp8_sdwa v105, v202 src0_sel:BYTE_3
	s_waitcnt vmcnt(16)
	v_cvt_f32_fp8_e32 v106, v203
	v_cvt_f32_fp8_sdwa v107, v203 src0_sel:BYTE_1
	v_add_f32_dpp v52, v52, v52 quad_perm:[1,0,3,2] row_mask:0xf bank_mask:0xf bound_ctrl:1
	v_mul_f32_e32 v53, 0x45800000, v74
	v_pk_fma_f32 v[138:139], v[28:29], v[54:55], 0 op_sel_hi:[0,1,0]
	v_add_f32_dpp v52, v52, v52 quad_perm:[2,3,0,1] row_mask:0xf bank_mask:0xf bound_ctrl:1
	s_waitcnt lgkmcnt(0)
	v_lshl_add_u64 v[54:55], s[10:11], 0, v[78:79]
	v_pk_fma_f32 v[140:141], v[28:29], v[96:97], 0 op_sel_hi:[0,1,0]
	v_add_f32_dpp v156, v52, v52 row_half_mirror row_mask:0xf bank_mask:0xf bound_ctrl:1
	v_cndmask_b32_e64 v52, v74, v53, s[2:3]
	v_pk_fma_f32 v[146:147], v[28:29], v[98:99], 0 op_sel_hi:[0,1,0]
	v_pk_mul_f32 v[96:97], v[128:129], v[52:53] op_sel_hi:[1,0]
	v_pk_mul_f32 v[98:99], v[120:121], v[52:53] op_sel_hi:[1,0]
	v_add_co_u32_e64 v120, s[2:3], s76, v54
	v_pk_fma_f32 v[148:149], v[28:29], v[100:101], 0 op_sel_hi:[0,1,0]
	v_pk_fma_f32 v[150:151], v[28:29], v[104:105], 0 op_sel_hi:[0,1,0]
	v_pk_fma_f32 v[152:153], v[28:29], v[102:103], 0 op_sel_hi:[0,1,0]
	v_pk_fma_f32 v[154:155], v[28:29], v[106:107], 0 op_sel_hi:[0,1,0]
	v_addc_co_u32_e64 v121, s[2:3], -1, v55, s[2:3]
	v_pk_mul_f32 v[100:101], v[122:123], v[52:53] op_sel_hi:[1,0]
	v_pk_mul_f32 v[102:103], v[114:115], v[52:53] op_sel_hi:[1,0]
	v_pk_mul_f32 v[104:105], v[124:125], v[52:53] op_sel_hi:[1,0]
	v_pk_mul_f32 v[106:107], v[116:117], v[52:53] op_sel_hi:[1,0]
	v_pk_mul_f32 v[114:115], v[126:127], v[52:53] op_sel_hi:[1,0]
	v_pk_mul_f32 v[116:117], v[118:119], v[52:53] op_sel_hi:[1,0]
	v_pk_mul_f32 v[54:55], v[2:3], v[98:99]
	v_pk_mul_f32 v[52:53], v[0:1], v[96:97]
	v_pk_mul_f32 v[98:99], v[6:7], v[102:103]
	v_pk_mul_f32 v[96:97], v[4:5], v[100:101]
	v_pk_mul_f32 v[102:103], v[10:11], v[106:107]
	v_pk_mul_f32 v[100:101], v[8:9], v[104:105]
	v_pk_mul_f32 v[106:107], v[14:15], v[116:117]
	v_pk_mul_f32 v[104:105], v[12:13], v[114:115]
	global_store_dwordx4 v[120:121], v[52:55], off offset:-3072
	global_store_dwordx4 v[120:121], v[96:99], off offset:-2048
	global_store_dwordx4 v[120:121], v[100:103], off offset:-1024
	global_store_dwordx4 v[120:121], v[104:107], off
	v_mbcnt_lo_u32_b32 v52, -1, 0
	v_mbcnt_hi_u32_b32 v52, -1, v52
	v_add_f32_dpp v74, v156, v156 row_mirror row_mask:0xf bank_mask:0xf bound_ctrl:1
	v_lshlrev_b32_e32 v52, 2, v52
	v_xor_b32_e32 v52, 64, v52
	ds_bpermute_b32 v114, v52, v74
	v_cvt_f32_fp8_sdwa v136, v203 src0_sel:BYTE_2
	v_cvt_f32_fp8_sdwa v137, v203 src0_sel:BYTE_3
	s_waitcnt vmcnt(19)
	v_cvt_f32_fp8_e32 v52, v204
	v_cvt_f32_fp8_sdwa v53, v204 src0_sel:BYTE_1
	v_cvt_f32_fp8_sdwa v54, v204 src0_sel:BYTE_2
	v_cvt_f32_fp8_sdwa v55, v204 src0_sel:BYTE_3
	s_waitcnt vmcnt(18)
	v_cvt_f32_fp8_e32 v96, v205
	v_cvt_f32_fp8_sdwa v97, v205 src0_sel:BYTE_1
	v_cvt_f32_fp8_sdwa v98, v205 src0_sel:BYTE_2
	v_cvt_f32_fp8_sdwa v99, v205 src0_sel:BYTE_3
	s_waitcnt vmcnt(17)
	v_cvt_f32_fp8_e32 v100, v206
	v_cvt_f32_fp8_sdwa v101, v206 src0_sel:BYTE_1
	v_cvt_f32_fp8_sdwa v102, v206 src0_sel:BYTE_2
	v_cvt_f32_fp8_sdwa v103, v206 src0_sel:BYTE_3
	s_waitcnt vmcnt(16)
	v_cvt_f32_fp8_e32 v104, v207
	v_cvt_f32_fp8_sdwa v105, v207 src0_sel:BYTE_1
	v_cvt_f32_fp8_sdwa v106, v207 src0_sel:BYTE_2
	v_cvt_f32_fp8_sdwa v107, v207 src0_sel:BYTE_3
	s_waitcnt lgkmcnt(0)
	v_add_f32_e32 v74, v74, v114
	s_mov_b32 s68, 34
	v_pk_fma_f32 v[136:137], v[28:29], v[136:137], 0 op_sel_hi:[0,1,0]
	v_mov_b32_e32 v156, v74
	v_pk_fma_f32 v[114:115], v[28:29], v[54:55], v[140:141] op_sel:[1,0,0]
	v_pk_fma_f32 v[116:117], v[28:29], v[52:53], v[138:139] op_sel:[1,0,0]
	v_pk_fma_f32 v[118:119], v[28:29], v[98:99], v[148:149] op_sel:[1,0,0]
	v_pk_fma_f32 v[120:121], v[28:29], v[96:97], v[146:147] op_sel:[1,0,0]
	v_pk_fma_f32 v[122:123], v[28:29], v[100:101], v[152:153] op_sel:[1,0,0]
	v_pk_fma_f32 v[124:125], v[28:29], v[102:103], v[150:151] op_sel:[1,0,0]
	v_pk_fma_f32 v[126:127], v[28:29], v[104:105], v[154:155] op_sel:[1,0,0]
	v_pk_fma_f32 v[128:129], v[28:29], v[106:107], v[136:137] op_sel:[1,0,0]
	s_nop 1
	v_permlane32_swap_b32 v74, v156
	v_mov_b64_e32 v[28:29], v[48:49]
	v_add_f32_e32 v48, v74, v156
	s_ashr_i32 s69, s68, 31
	v_fmamk_f32 v48, v48, 0x3a800000, v73
	s_lshl_b64 s[10:11], s[68:69], 3
	v_mul_f32_e32 v49, 0x4b800000, v48
	s_add_u32 s10, s0, s10
	v_cmp_gt_f32_e64 s[2:3], s74, v48
	s_addc_u32 s11, s1, s11
	s_load_dwordx2 s[10:11], s[10:11], 0x0
	v_cndmask_b32_e64 v48, v48, v49, s[2:3]
	v_rsq_f32_e32 v52, v48
	s_waitcnt vmcnt(15)
	v_cvt_f32_fp8_e32 v48, v208
	v_cvt_f32_fp8_sdwa v49, v208 src0_sel:BYTE_1
	s_waitcnt lgkmcnt(0)
	v_lshl_add_u64 v[154:155], s[10:11], 0, v[78:79]
	v_mul_f32_e32 v53, 0x45800000, v52
	v_cndmask_b32_e64 v52, v52, v53, s[2:3]
	s_waitcnt vmcnt(13)
	v_cvt_f32_fp8_e32 v146, v210
	v_cvt_f32_fp8_sdwa v147, v210 src0_sel:BYTE_1
	v_pk_mul_f32 v[96:97], v[142:143], v[52:53] op_sel_hi:[1,0]
	v_pk_mul_f32 v[54:55], v[130:131], v[52:53] op_sel_hi:[1,0]
	v_add_co_u32_e64 v130, s[2:3], s73, v154
	v_pk_mul_f32 v[100:101], v[132:133], v[52:53] op_sel_hi:[1,0]
	s_nop 0
	v_addc_co_u32_e64 v131, s[2:3], -1, v155, s[2:3]
	v_pk_mul_f32 v[98:99], v[144:145], v[52:53] op_sel_hi:[1,0]
	v_pk_mul_f32 v[104:105], v[134:135], v[52:53] op_sel_hi:[1,0]
	v_pk_mul_f32 v[102:103], v[110:111], v[52:53] op_sel_hi:[1,0]
	v_pk_mul_f32 v[108:109], v[108:109], v[52:53] op_sel_hi:[1,0]
	v_pk_mul_f32 v[106:107], v[112:113], v[52:53] op_sel_hi:[1,0]
	v_pk_mul_f32 v[54:55], v[2:3], v[54:55]
	v_pk_mul_f32 v[52:53], v[0:1], v[96:97]
	v_pk_mul_f32 v[98:99], v[6:7], v[98:99]
	v_pk_mul_f32 v[96:97], v[4:5], v[100:101]
	v_pk_mul_f32 v[102:103], v[10:11], v[102:103]
	v_pk_mul_f32 v[100:101], v[8:9], v[104:105]
	v_pk_mul_f32 v[106:107], v[14:15], v[106:107]
	v_pk_mul_f32 v[104:105], v[12:13], v[108:109]
	global_store_dwordx4 v[130:131], v[52:55], off offset:-3072
	global_store_dwordx4 v[130:131], v[96:99], off offset:-2048
	global_store_dwordx4 v[130:131], v[100:103], off offset:-1024
	global_store_dwordx4 v[154:155], v[104:107], off offset:-4096
	v_mbcnt_lo_u32_b32 v52, -1, 0
	v_mbcnt_hi_u32_b32 v52, -1, v52
	v_cvt_f32_fp8_sdwa v136, v208 src0_sel:BYTE_2
	v_cvt_f32_fp8_sdwa v137, v208 src0_sel:BYTE_3
	v_cvt_f32_fp8_e32 v138, v209
	v_cvt_f32_fp8_sdwa v139, v209 src0_sel:BYTE_1
	v_cvt_f32_fp8_sdwa v140, v209 src0_sel:BYTE_2
	v_cvt_f32_fp8_sdwa v141, v209 src0_sel:BYTE_3
	v_lshlrev_b32_e32 v52, 2, v52
	v_cvt_f32_fp8_sdwa v148, v210 src0_sel:BYTE_2
	v_cvt_f32_fp8_sdwa v149, v210 src0_sel:BYTE_3
	s_waitcnt vmcnt(16)
	v_cvt_f32_fp8_e32 v150, v227
	v_cvt_f32_fp8_sdwa v151, v227 src0_sel:BYTE_1
	v_cvt_f32_fp8_sdwa v152, v227 src0_sel:BYTE_2
	v_cvt_f32_fp8_sdwa v153, v227 src0_sel:BYTE_3
	v_pk_fma_f32 v[48:49], v[30:31], v[48:49], v[116:117] op_sel_hi:[0,1,1]
	v_pk_fma_f32 v[116:117], v[30:31], v[146:147], v[122:123] op_sel_hi:[0,1,1]
	v_xor_b32_e32 v122, 64, v52
	s_waitcnt vmcnt(15)
	v_cvt_f32_fp8_e32 v52, v178
	v_cvt_f32_fp8_sdwa v53, v178 src0_sel:BYTE_1
	v_cvt_f32_fp8_sdwa v54, v178 src0_sel:BYTE_2
	v_cvt_f32_fp8_sdwa v55, v178 src0_sel:BYTE_3
	s_waitcnt vmcnt(14)
	v_cvt_f32_fp8_e32 v96, v179
	v_cvt_f32_fp8_sdwa v97, v179 src0_sel:BYTE_1
	v_cvt_f32_fp8_sdwa v98, v179 src0_sel:BYTE_2
	v_cvt_f32_fp8_sdwa v99, v179 src0_sel:BYTE_3
	s_waitcnt vmcnt(13)
	v_cvt_f32_fp8_e32 v100, v180
	v_cvt_f32_fp8_sdwa v101, v180 src0_sel:BYTE_1
	v_cvt_f32_fp8_sdwa v102, v180 src0_sel:BYTE_2
	v_cvt_f32_fp8_sdwa v103, v180 src0_sel:BYTE_3
	s_waitcnt vmcnt(12)
	v_cvt_f32_fp8_e32 v104, v181
	v_cvt_f32_fp8_sdwa v105, v181 src0_sel:BYTE_1
	v_cvt_f32_fp8_sdwa v106, v181 src0_sel:BYTE_2
	v_cvt_f32_fp8_sdwa v107, v181 src0_sel:BYTE_3
	v_pk_fma_f32 v[108:109], v[30:31], v[136:137], v[114:115] op_sel_hi:[0,1,1]
	v_pk_fma_f32 v[110:111], v[30:31], v[138:139], v[120:121] op_sel_hi:[0,1,1]
	v_pk_fma_f32 v[112:113], v[30:31], v[140:141], v[118:119] op_sel_hi:[0,1,1]
	v_pk_fma_f32 v[114:115], v[30:31], v[148:149], v[124:125] op_sel_hi:[0,1,1]
	v_pk_fma_f32 v[118:119], v[30:31], v[152:153], v[128:129] op_sel_hi:[0,1,1]
	v_pk_fma_f32 v[120:121], v[30:31], v[150:151], v[126:127] op_sel_hi:[0,1,1]
	v_pk_fma_f32 v[54:55], v[30:31], v[54:55], v[108:109] op_sel:[1,0,0]
	v_pk_fma_f32 v[48:49], v[30:31], v[52:53], v[48:49] op_sel:[1,0,0]
	v_pk_fma_f32 v[52:53], v[30:31], v[98:99], v[112:113] op_sel:[1,0,0]
	v_pk_fma_f32 v[96:97], v[30:31], v[96:97], v[110:111] op_sel:[1,0,0]
	v_pk_fma_f32 v[98:99], v[30:31], v[100:101], v[116:117] op_sel:[1,0,0]
	v_pk_fma_f32 v[100:101], v[30:31], v[102:103], v[114:115] op_sel:[1,0,0]
	v_pk_fma_f32 v[102:103], v[30:31], v[104:105], v[120:121] op_sel:[1,0,0]
	v_pk_fma_f32 v[104:105], v[30:31], v[106:107], v[118:119] op_sel:[1,0,0]
	v_mov_b64_e32 v[30:31], v[50:51]
	v_pk_fma_f32 v[48:49], v[68:69], v[48:49], v[80:81]
	v_pk_fma_f32 v[50:51], v[70:71], v[54:55], v[82:83]
	v_pk_fma_f32 v[54:55], v[64:65], v[96:97], v[84:85]
	v_pk_fma_f32 v[52:53], v[66:67], v[52:53], v[88:89]
	v_pk_mul_f32 v[64:65], v[50:51], v[50:51]
	v_pk_mul_f32 v[66:67], v[48:49], v[48:49]
	v_pk_mul_f32 v[68:69], v[52:53], v[52:53]
	v_pk_mul_f32 v[70:71], v[54:55], v[54:55]
	v_pk_fma_f32 v[62:63], v[62:63], v[100:101], v[92:93]
	v_pk_fma_f32 v[60:61], v[60:61], v[98:99], v[86:87]
	v_pk_mov_b32 v[82:83], v[66:67], v[64:65] op_sel:[1,0]
	v_mov_b32_e32 v67, v65
	v_pk_mov_b32 v[64:65], v[70:71], v[68:69] op_sel:[1,0]
	v_mov_b32_e32 v71, v69
	v_pk_fma_f32 v[58:59], v[58:59], v[104:105], v[94:95]
	v_pk_fma_f32 v[56:57], v[56:57], v[102:103], v[90:91]
	v_mul_f32_e32 v74, v61, v61
	v_mul_f32_e32 v80, v63, v63
	v_pk_add_f32 v[66:67], v[82:83], v[66:67]
	v_pk_add_f32 v[64:65], v[64:65], v[70:71]
	v_mul_f32_e32 v84, v56, v56
	v_mul_f32_e32 v85, v57, v57
	v_mul_f32_e32 v86, v58, v58
	v_mul_f32_e32 v87, v59, v59
	v_pk_fma_f32 v[68:69], v[60:61], v[60:61], v[74:75] op_sel_hi:[1,1,0]
	v_pk_fma_f32 v[80:81], v[62:63], v[62:63], v[80:81] op_sel_hi:[1,1,0]
	v_pk_add_f32 v[66:67], v[66:67], v[66:67] op_sel:[0,1] op_sel_hi:[1,0]
	v_pk_add_f32 v[64:65], v[64:65], v[64:65] op_sel:[0,1] op_sel_hi:[1,0]
	v_mov_b32_e32 v69, v86
	v_mov_b32_e32 v81, v87
	v_mov_b32_e32 v67, v84
	v_mov_b32_e32 v65, v85
	v_pk_add_f32 v[68:69], v[68:69], v[80:81]
	v_pk_add_f32 v[64:65], v[66:67], v[64:65]
	s_mov_b32 s62, 34
	v_pk_add_f32 v[64:65], v[64:65], v[68:69]
	s_nop 0
	v_add_f32_e32 v64, v64, v65
	s_nop 1
	v_add_f32_dpp v64, v64, v64 quad_perm:[1,0,3,2] row_mask:0xf bank_mask:0xf bound_ctrl:1
	s_nop 1
	v_add_f32_dpp v64, v64, v64 quad_perm:[2,3,0,1] row_mask:0xf bank_mask:0xf bound_ctrl:1
	s_nop 1
	v_add_f32_dpp v64, v64, v64 row_half_mirror row_mask:0xf bank_mask:0xf bound_ctrl:1
	s_nop 1
	v_add_f32_dpp v64, v64, v64 row_mirror row_mask:0xf bank_mask:0xf bound_ctrl:1
	ds_bpermute_b32 v65, v122, v64
	s_waitcnt lgkmcnt(0)
	v_add_f32_e32 v64, v64, v65
	v_mov_b32_e32 v65, v64
	s_nop 1
	v_permlane32_swap_b32 v65, v64
	s_ashr_i32 s63, s62, 31
	v_add_f32_e32 v64, v65, v64
	v_fmamk_f32 v64, v64, 0x3a800000, v73
	v_mul_f32_e32 v65, 0x4b800000, v64
	v_cmp_gt_f32_e64 s[2:3], s74, v64
	s_lshl_b64 s[10:11], s[62:63], 3
	s_add_u32 s10, s0, s10
	v_cndmask_b32_e64 v64, v64, v65, s[2:3]
	v_rsq_f32_e32 v64, v64
	s_addc_u32 s11, s1, s11
	s_load_dwordx2 s[10:11], s[10:11], 0x0
	s_or_b64 s[6:7], vcc, s[6:7]
	v_mul_f32_e32 v65, 0x45800000, v64
	v_cndmask_b32_e64 v64, v64, v65, s[2:3]
	v_pk_mul_f32 v[48:49], v[48:49], v[64:65] op_sel_hi:[1,0]
	v_pk_mul_f32 v[50:51], v[50:51], v[64:65] op_sel_hi:[1,0]
	s_waitcnt lgkmcnt(0)
	v_lshl_add_u64 v[66:67], s[10:11], 0, v[78:79]
	v_lshl_add_u64 v[78:79], v[78:79], 0, s[4:5]
	v_pk_mul_f32 v[68:69], v[54:55], v[64:65] op_sel_hi:[1,0]
	v_pk_mul_f32 v[52:53], v[52:53], v[64:65] op_sel_hi:[1,0]
	v_pk_mul_f32 v[60:61], v[60:61], v[64:65] op_sel_hi:[1,0]
	v_pk_mul_f32 v[62:63], v[62:63], v[64:65] op_sel_hi:[1,0]
	v_pk_mul_f32 v[70:71], v[56:57], v[64:65] op_sel_hi:[1,0]
	v_pk_mul_f32 v[64:65], v[58:59], v[64:65] op_sel_hi:[1,0]
	v_pk_mul_f32 v[50:51], v[2:3], v[50:51]
	v_pk_mul_f32 v[48:49], v[0:1], v[48:49]
	v_pk_mul_f32 v[54:55], v[6:7], v[52:53]
	v_pk_mul_f32 v[52:53], v[4:5], v[68:69]
	v_pk_mul_f32 v[58:59], v[10:11], v[62:63]
	v_pk_mul_f32 v[56:57], v[8:9], v[60:61]
	v_pk_mul_f32 v[62:63], v[14:15], v[64:65]
	v_pk_mul_f32 v[60:61], v[12:13], v[70:71]
	global_store_dwordx4 v[66:67], v[48:51], off offset:-3072
	global_store_dwordx4 v[66:67], v[52:55], off offset:-2048
	global_store_dwordx4 v[66:67], v[56:59], off offset:-1024
	global_store_dwordx4 v[66:67], v[60:63], off
	s_andn2_b64 exec, exec, s[6:7]
	s_cbranch_execnz .LBB0_1977
